# first-iteration peel with C=0 MFMAs extended to all 13 GEMM K loops (no accumulator zeroing anywhere)
# speedup vs baseline: 1.0093x; 1.0009x over previous
.LBB0_227:
	s_ashr_i32 s47, s46, 31
	s_lshl_b64 s[50:51], s[46:47], 19
	s_add_u32 s50, s21, s50
	s_addc_u32 s51, s22, s51
	s_ashr_i32 s43, s42, 31
	s_lshl_b64 s[52:53], s[42:43], 19
	s_add_u32 s52, s15, s52
	s_addc_u32 s53, s20, s53
	s_andn2_b64 vcc, exec, s[30:31]
	s_cbranch_vccnz .LBB0_269
	s_and_b64 s[62:63], s[48:49], exec
	s_cselect_b32 s39, s51, s59
	s_cselect_b32 s43, s50, s58
	s_cselect_b32 s47, s53, s61
	s_cselect_b32 s55, s52, s60
	s_add_u32 s71, s60, 0x100
	s_addc_u32 s72, s61, 0
	s_add_u32 s58, s58, 0x40080
	v_mov_b32_e32 v1, 0x3ecc95a3
	s_addc_u32 s59, s59, 0
	s_mov_b32 s60, 0
.Lpeelph1b_0:
	s_add_i32 s73, s60, 2
	s_add_u32 s61, s58, 0xfffc0080
	s_addc_u32 s62, s59, -1
	s_add_i32 s74, 0, 0x10000
	s_cmp_eq_u32 s68, s60
	s_cselect_b32 s63, s39, s62
	s_cselect_b32 s62, s43, s61
	s_cselect_b32 s61, s47, s72
	s_cselect_b32 s60, s55, s71
	s_add_i32 s76, 0, 0x14000
	v_add_u32_e32 v156, s74, v165
	v_add_u32_e32 v166, s76, v165
	ds_read_b128 v[144:147], v156
	ds_read_b128 v[148:151], v156 offset:1024
	ds_read_b128 v[152:155], v156 offset:2048
	ds_read_b128 v[156:159], v156 offset:3072
	ds_read_b128 v[160:163], v166
	ds_read_b128 v[170:173], v166 offset:1024
	ds_read_b128 v[174:177], v166 offset:2048
	ds_read_b128 v[180:183], v166 offset:3072
	v_lshl_add_u64 v[216:217], s[58:59], 0, v[142:143]
	s_add_i32 m0, s8, 0xc000
	ds_read_b128 v[184:187], v178
	ds_read_b128 v[188:191], v178 offset:1024
	ds_read_b128 v[192:195], v178 offset:2048
	ds_read_b128 v[196:199], v178 offset:3072
	ds_read_b128 v[200:203], v178 offset:4096
	ds_read_b128 v[204:207], v178 offset:5120
	ds_read_b128 v[208:211], v178 offset:6144
	ds_read_b128 v[212:215], v178 offset:7168
	global_load_lds_dwordx4 v[216:217], off
	v_lshl_add_u64 v[216:217], s[58:59], 0, v[140:141]
	s_add_i32 m0, s8, 0xe000
	s_nop 0
	global_load_lds_dwordx4 v[216:217], off
	s_waitcnt vmcnt(8)
	s_waitcnt lgkmcnt(0)
	s_barrier
	s_setprio 1
	s_waitcnt lgkmcnt(0)
	v_mfma_f32_16x16x32_bf16 v[126:129], v[144:147], v[184:187], 0
	v_mfma_f32_16x16x32_bf16 v[122:125], v[152:155], v[184:187], 0
	v_mfma_f32_16x16x32_bf16 v[110:113], v[144:147], v[192:195], 0
	v_mfma_f32_16x16x32_bf16 v[106:109], v[152:155], v[192:195], 0
	v_mfma_f32_16x16x32_bf16 v[94:97], v[144:147], v[200:203], 0
	v_mfma_f32_16x16x32_bf16 v[90:93], v[152:155], v[200:203], 0
	v_mfma_f32_16x16x32_bf16 v[78:81], v[144:147], v[208:211], 0
	v_mfma_f32_16x16x32_bf16 v[74:77], v[152:155], v[208:211], 0
	v_mfma_f32_16x16x32_bf16 v[126:129], v[148:151], v[188:191], v[126:129]
	v_mfma_f32_16x16x32_bf16 v[122:125], v[156:159], v[188:191], v[122:125]
	v_mfma_f32_16x16x32_bf16 v[110:113], v[148:151], v[196:199], v[110:113]
	v_mfma_f32_16x16x32_bf16 v[106:109], v[156:159], v[196:199], v[106:109]
	v_mfma_f32_16x16x32_bf16 v[94:97], v[148:151], v[204:207], v[94:97]
	v_mfma_f32_16x16x32_bf16 v[90:93], v[156:159], v[204:207], v[90:93]
	v_mfma_f32_16x16x32_bf16 v[78:81], v[148:151], v[212:215], v[78:81]
	v_mfma_f32_16x16x32_bf16 v[74:77], v[156:159], v[212:215], v[74:77]
	s_setprio 0
	s_setprio 1
	v_mfma_f32_16x16x32_bf16 v[118:121], v[160:163], v[184:187], 0
	v_mfma_f32_16x16x32_bf16 v[114:117], v[174:177], v[184:187], 0
	v_mfma_f32_16x16x32_bf16 v[102:105], v[160:163], v[192:195], 0
	v_mfma_f32_16x16x32_bf16 v[98:101], v[174:177], v[192:195], 0
	v_mfma_f32_16x16x32_bf16 v[86:89], v[160:163], v[200:203], 0
	v_mfma_f32_16x16x32_bf16 v[82:85], v[174:177], v[200:203], 0
	v_mfma_f32_16x16x32_bf16 v[70:73], v[160:163], v[208:211], 0
	v_mfma_f32_16x16x32_bf16 v[66:69], v[174:177], v[208:211], 0
	v_mfma_f32_16x16x32_bf16 v[118:121], v[170:173], v[188:191], v[118:121]
	v_mfma_f32_16x16x32_bf16 v[114:117], v[180:183], v[188:191], v[114:117]
	v_mfma_f32_16x16x32_bf16 v[102:105], v[170:173], v[196:199], v[102:105]
	v_mfma_f32_16x16x32_bf16 v[98:101], v[180:183], v[196:199], v[98:101]
	v_mfma_f32_16x16x32_bf16 v[86:89], v[170:173], v[204:207], v[86:89]
	v_mfma_f32_16x16x32_bf16 v[82:85], v[180:183], v[204:207], v[82:85]
	v_mfma_f32_16x16x32_bf16 v[70:73], v[170:173], v[212:215], v[70:73]
	v_mfma_f32_16x16x32_bf16 v[66:69], v[180:183], v[212:215], v[66:69]
	s_setprio 0
	s_barrier
	s_add_i32 s74, s74, s1
	v_lshl_add_u64 v[216:217], s[60:61], 0, v[130:131]
	s_mov_b32 m0, s74
	ds_read_b128 v[184:187], v178 offset:16384
	ds_read_b128 v[188:191], v178 offset:17408
	ds_read_b128 v[192:195], v178 offset:18432
	ds_read_b128 v[196:199], v178 offset:19456
	ds_read_b128 v[200:203], v178 offset:20480
	ds_read_b128 v[204:207], v178 offset:21504
	ds_read_b128 v[208:211], v178 offset:22528
	ds_read_b128 v[212:215], v178 offset:23552
	global_load_lds_dwordx4 v[216:217], off
	s_add_i32 m0, s74, 0x2000
	s_add_u32 s74, s60, 0x40000
	v_lshl_add_u64 v[218:219], s[60:61], 0, v[132:133]
	s_addc_u32 s75, s61, 0
	s_add_i32 s76, s76, s1
	global_load_lds_dwordx4 v[218:219], off
	v_lshl_add_u64 v[220:221], s[74:75], 0, v[130:131]
	s_mov_b32 m0, s76
	v_lshl_add_u64 v[222:223], s[62:63], 0, v[136:137]
	global_load_lds_dwordx4 v[220:221], off
	v_lshl_add_u64 v[220:221], s[74:75], 0, v[132:133]
	s_add_i32 m0, s76, 0x2000
	s_nop 0
	global_load_lds_dwordx4 v[220:221], off
	v_lshl_add_u64 v[220:221], s[62:63], 0, v[134:135]
	s_mov_b32 m0, s8
	s_nop 0
	global_load_lds_dwordx4 v[220:221], off
	s_mov_b32 m0, s11
	s_nop 0
	global_load_lds_dwordx4 v[222:223], off
	s_waitcnt vmcnt(8)
	s_waitcnt lgkmcnt(0)
	s_barrier
	s_setprio 1
	s_waitcnt lgkmcnt(0)
	v_mfma_f32_16x16x32_bf16 v[62:65], v[144:147], v[184:187], 0
	v_mfma_f32_16x16x32_bf16 v[58:61], v[152:155], v[184:187], 0
	v_mfma_f32_16x16x32_bf16 v[46:49], v[144:147], v[192:195], 0
	v_mfma_f32_16x16x32_bf16 v[42:45], v[152:155], v[192:195], 0
	v_mfma_f32_16x16x32_bf16 v[30:33], v[144:147], v[200:203], 0
	v_mfma_f32_16x16x32_bf16 v[26:29], v[152:155], v[200:203], 0
	v_mfma_f32_16x16x32_bf16 v[14:17], v[144:147], v[208:211], 0
	v_mfma_f32_16x16x32_bf16 v[10:13], v[152:155], v[208:211], 0
	v_mfma_f32_16x16x32_bf16 v[62:65], v[148:151], v[188:191], v[62:65]
	v_mfma_f32_16x16x32_bf16 v[58:61], v[156:159], v[188:191], v[58:61]
	v_mfma_f32_16x16x32_bf16 v[46:49], v[148:151], v[196:199], v[46:49]
	v_mfma_f32_16x16x32_bf16 v[42:45], v[156:159], v[196:199], v[42:45]
	v_mfma_f32_16x16x32_bf16 v[30:33], v[148:151], v[204:207], v[30:33]
	v_mfma_f32_16x16x32_bf16 v[26:29], v[156:159], v[204:207], v[26:29]
	v_mfma_f32_16x16x32_bf16 v[14:17], v[148:151], v[212:215], v[14:17]
	v_mfma_f32_16x16x32_bf16 v[10:13], v[156:159], v[212:215], v[10:13]
	s_setprio 0
	s_setprio 1
	v_mfma_f32_16x16x32_bf16 v[54:57], v[160:163], v[184:187], 0
	v_mfma_f32_16x16x32_bf16 v[50:53], v[174:177], v[184:187], 0
	v_mfma_f32_16x16x32_bf16 v[38:41], v[160:163], v[192:195], 0
	v_mfma_f32_16x16x32_bf16 v[34:37], v[174:177], v[192:195], 0
	v_mfma_f32_16x16x32_bf16 v[22:25], v[160:163], v[200:203], 0
	v_mfma_f32_16x16x32_bf16 v[18:21], v[174:177], v[200:203], 0
	v_mfma_f32_16x16x32_bf16 v[6:9], v[160:163], v[208:211], 0
	v_mfma_f32_16x16x32_bf16 v[2:5], v[174:177], v[208:211], 0
	v_mfma_f32_16x16x32_bf16 v[54:57], v[170:173], v[188:191], v[54:57]
	v_mfma_f32_16x16x32_bf16 v[50:53], v[180:183], v[188:191], v[50:53]
	v_mfma_f32_16x16x32_bf16 v[38:41], v[170:173], v[196:199], v[38:41]
	v_mfma_f32_16x16x32_bf16 v[34:37], v[180:183], v[196:199], v[34:37]
	v_mfma_f32_16x16x32_bf16 v[22:25], v[170:173], v[204:207], v[22:25]
	v_mfma_f32_16x16x32_bf16 v[18:21], v[180:183], v[204:207], v[18:21]
	v_mfma_f32_16x16x32_bf16 v[6:9], v[170:173], v[212:215], v[6:9]
	v_mfma_f32_16x16x32_bf16 v[2:5], v[180:183], v[212:215], v[2:5]
	s_setprio 0
	s_barrier
	s_add_i32 s74, 0, 0x18000
	s_add_i32 s75, 0, 0x1c000
	v_add_u32_e32 v156, s74, v165
	v_add_u32_e32 v166, s75, v165
	ds_read_b128 v[144:147], v156
	ds_read_b128 v[148:151], v156 offset:1024
	ds_read_b128 v[152:155], v156 offset:2048
	ds_read_b128 v[156:159], v156 offset:3072
	ds_read_b128 v[160:163], v166
	ds_read_b128 v[170:173], v166 offset:1024
	ds_read_b128 v[174:177], v166 offset:2048
	ds_read_b128 v[180:183], v166 offset:3072
	s_add_u32 s62, s62, 0x40000
	s_addc_u32 s63, s63, 0
	s_mov_b32 m0, s16
	v_lshl_add_u64 v[232:233], s[62:63], 0, v[134:135]
	ds_read_b128 v[184:187], v178 offset:32768
	ds_read_b128 v[188:191], v178 offset:33792
	ds_read_b128 v[192:195], v178 offset:34816
	ds_read_b128 v[196:199], v178 offset:35840
	ds_read_b128 v[200:203], v178 offset:36864
	ds_read_b128 v[204:207], v178 offset:37888
	ds_read_b128 v[208:211], v178 offset:38912
	ds_read_b128 v[212:215], v178 offset:39936
	global_load_lds_dwordx4 v[232:233], off
	v_lshl_add_u64 v[232:233], s[62:63], 0, v[136:137]
	s_mov_b32 m0, s25
	s_nop 0
	global_load_lds_dwordx4 v[232:233], off
	s_waitcnt vmcnt(8)
	s_waitcnt lgkmcnt(0)
	s_barrier
	s_setprio 1
	s_waitcnt lgkmcnt(0)
	v_mfma_f32_16x16x32_bf16 v[126:129], v[144:147], v[184:187], v[126:129]
	v_mfma_f32_16x16x32_bf16 v[122:125], v[152:155], v[184:187], v[122:125]
	v_mfma_f32_16x16x32_bf16 v[110:113], v[144:147], v[192:195], v[110:113]
	v_mfma_f32_16x16x32_bf16 v[106:109], v[152:155], v[192:195], v[106:109]
	v_mfma_f32_16x16x32_bf16 v[94:97], v[144:147], v[200:203], v[94:97]
	v_mfma_f32_16x16x32_bf16 v[90:93], v[152:155], v[200:203], v[90:93]
	v_mfma_f32_16x16x32_bf16 v[78:81], v[144:147], v[208:211], v[78:81]
	v_mfma_f32_16x16x32_bf16 v[74:77], v[152:155], v[208:211], v[74:77]
	v_mfma_f32_16x16x32_bf16 v[126:129], v[148:151], v[188:191], v[126:129]
	v_mfma_f32_16x16x32_bf16 v[122:125], v[156:159], v[188:191], v[122:125]
	v_mfma_f32_16x16x32_bf16 v[110:113], v[148:151], v[196:199], v[110:113]
	v_mfma_f32_16x16x32_bf16 v[106:109], v[156:159], v[196:199], v[106:109]
	v_mfma_f32_16x16x32_bf16 v[94:97], v[148:151], v[204:207], v[94:97]
	v_mfma_f32_16x16x32_bf16 v[90:93], v[156:159], v[204:207], v[90:93]
	v_mfma_f32_16x16x32_bf16 v[78:81], v[148:151], v[212:215], v[78:81]
	v_mfma_f32_16x16x32_bf16 v[74:77], v[156:159], v[212:215], v[74:77]
	s_setprio 0
	s_setprio 1
	v_mfma_f32_16x16x32_bf16 v[118:121], v[160:163], v[184:187], v[118:121]
	v_mfma_f32_16x16x32_bf16 v[114:117], v[174:177], v[184:187], v[114:117]
	v_mfma_f32_16x16x32_bf16 v[102:105], v[160:163], v[192:195], v[102:105]
	v_mfma_f32_16x16x32_bf16 v[98:101], v[174:177], v[192:195], v[98:101]
	v_mfma_f32_16x16x32_bf16 v[86:89], v[160:163], v[200:203], v[86:89]
	v_mfma_f32_16x16x32_bf16 v[82:85], v[174:177], v[200:203], v[82:85]
	v_mfma_f32_16x16x32_bf16 v[70:73], v[160:163], v[208:211], v[70:73]
	v_mfma_f32_16x16x32_bf16 v[66:69], v[174:177], v[208:211], v[66:69]
	v_mfma_f32_16x16x32_bf16 v[118:121], v[170:173], v[188:191], v[118:121]
	v_mfma_f32_16x16x32_bf16 v[114:117], v[180:183], v[188:191], v[114:117]
	v_mfma_f32_16x16x32_bf16 v[102:105], v[170:173], v[196:199], v[102:105]
	v_mfma_f32_16x16x32_bf16 v[98:101], v[180:183], v[196:199], v[98:101]
	v_mfma_f32_16x16x32_bf16 v[86:89], v[170:173], v[204:207], v[86:89]
	v_mfma_f32_16x16x32_bf16 v[82:85], v[180:183], v[204:207], v[82:85]
	v_mfma_f32_16x16x32_bf16 v[70:73], v[170:173], v[212:215], v[70:73]
	v_mfma_f32_16x16x32_bf16 v[66:69], v[180:183], v[212:215], v[66:69]
	s_setprio 0
	s_barrier
	s_add_i32 s62, s74, s1
	v_lshl_add_u64 v[216:217], v[216:217], 0, s[56:57]
	s_mov_b32 m0, s62
	ds_read_b128 v[184:187], v178 offset:49152
	ds_read_b128 v[188:191], v178 offset:50176
	ds_read_b128 v[192:195], v178 offset:51200
	ds_read_b128 v[196:199], v178 offset:52224
	ds_read_b128 v[200:203], v178 offset:53248
	ds_read_b128 v[204:207], v178 offset:54272
	ds_read_b128 v[208:211], v178 offset:55296
	ds_read_b128 v[212:215], v178 offset:56320
	global_load_lds_dwordx4 v[216:217], off
	s_add_i32 m0, s62, 0x2000
	s_add_u32 s60, s60, 0x40080
	v_lshl_add_u64 v[216:217], v[218:219], 0, s[56:57]
	s_addc_u32 s61, s61, 0
	s_add_i32 s62, s75, s1
	global_load_lds_dwordx4 v[216:217], off
	v_lshl_add_u64 v[216:217], s[60:61], 0, v[130:131]
	s_mov_b32 m0, s62
	s_nop 0
	global_load_lds_dwordx4 v[216:217], off
	v_lshl_add_u64 v[216:217], s[60:61], 0, v[132:133]
	s_add_i32 m0, s62, 0x2000
	s_nop 0
	global_load_lds_dwordx4 v[216:217], off
	v_lshl_add_u64 v[216:217], v[220:221], 0, s[56:57]
	s_mov_b32 m0, s64
	s_nop 0
	global_load_lds_dwordx4 v[216:217], off
	v_lshl_add_u64 v[216:217], v[222:223], 0, s[56:57]
	s_mov_b32 m0, s65
	s_nop 0
	global_load_lds_dwordx4 v[216:217], off
	s_waitcnt vmcnt(8)
	s_waitcnt lgkmcnt(0)
	s_barrier
	s_setprio 1
	s_waitcnt lgkmcnt(0)
	v_mfma_f32_16x16x32_bf16 v[62:65], v[144:147], v[184:187], v[62:65]
	v_mfma_f32_16x16x32_bf16 v[58:61], v[152:155], v[184:187], v[58:61]
	v_mfma_f32_16x16x32_bf16 v[46:49], v[144:147], v[192:195], v[46:49]
	v_mfma_f32_16x16x32_bf16 v[42:45], v[152:155], v[192:195], v[42:45]
	v_mfma_f32_16x16x32_bf16 v[30:33], v[144:147], v[200:203], v[30:33]
	v_mfma_f32_16x16x32_bf16 v[26:29], v[152:155], v[200:203], v[26:29]
	v_mfma_f32_16x16x32_bf16 v[14:17], v[144:147], v[208:211], v[14:17]
	v_mfma_f32_16x16x32_bf16 v[10:13], v[152:155], v[208:211], v[10:13]
	v_mfma_f32_16x16x32_bf16 v[62:65], v[148:151], v[188:191], v[62:65]
	v_mfma_f32_16x16x32_bf16 v[58:61], v[156:159], v[188:191], v[58:61]
	v_mfma_f32_16x16x32_bf16 v[46:49], v[148:151], v[196:199], v[46:49]
	v_mfma_f32_16x16x32_bf16 v[42:45], v[156:159], v[196:199], v[42:45]
	v_mfma_f32_16x16x32_bf16 v[30:33], v[148:151], v[204:207], v[30:33]
	v_mfma_f32_16x16x32_bf16 v[26:29], v[156:159], v[204:207], v[26:29]
	v_mfma_f32_16x16x32_bf16 v[14:17], v[148:151], v[212:215], v[14:17]
	v_mfma_f32_16x16x32_bf16 v[10:13], v[156:159], v[212:215], v[10:13]
	s_setprio 0
	s_setprio 1
	v_mfma_f32_16x16x32_bf16 v[54:57], v[160:163], v[184:187], v[54:57]
	v_mfma_f32_16x16x32_bf16 v[50:53], v[174:177], v[184:187], v[50:53]
	v_mfma_f32_16x16x32_bf16 v[38:41], v[160:163], v[192:195], v[38:41]
	v_mfma_f32_16x16x32_bf16 v[34:37], v[174:177], v[192:195], v[34:37]
	v_mfma_f32_16x16x32_bf16 v[22:25], v[160:163], v[200:203], v[22:25]
	v_mfma_f32_16x16x32_bf16 v[18:21], v[174:177], v[200:203], v[18:21]
	v_mfma_f32_16x16x32_bf16 v[6:9], v[160:163], v[208:211], v[6:9]
	v_mfma_f32_16x16x32_bf16 v[2:5], v[174:177], v[208:211], v[2:5]
	v_mfma_f32_16x16x32_bf16 v[54:57], v[170:173], v[188:191], v[54:57]
	v_mfma_f32_16x16x32_bf16 v[50:53], v[180:183], v[188:191], v[50:53]
	v_mfma_f32_16x16x32_bf16 v[38:41], v[170:173], v[196:199], v[38:41]
	v_mfma_f32_16x16x32_bf16 v[34:37], v[180:183], v[196:199], v[34:37]
	v_mfma_f32_16x16x32_bf16 v[22:25], v[170:173], v[204:207], v[22:25]
	v_mfma_f32_16x16x32_bf16 v[18:21], v[180:183], v[204:207], v[18:21]
	v_mfma_f32_16x16x32_bf16 v[6:9], v[170:173], v[212:215], v[6:9]
	v_mfma_f32_16x16x32_bf16 v[2:5], v[180:183], v[212:215], v[2:5]
	s_setprio 0
	s_barrier
	s_add_u32 s71, s71, 0x100
	s_addc_u32 s72, s72, 0
	s_add_u32 s58, s58, 0x100
	s_addc_u32 s59, s59, 0
	s_cmp_ge_i32 s73, s0
	s_mov_b32 s60, s73
	s_cbranch_scc0 .LBB0_229
	s_branch .Lpeelexitph1b

.Lpeelexitph1b:
	s_mov_b64 s[72:73], 0xe800000
	v_mov_b32_e32 v209, v1
	s_and_b64 vcc, exec, s[34:35]
	s_cbranch_vccz .LBB0_232

.LBB0_296:
	s_ashr_i32 s43, s42, 31
	s_lshl_b64 s[48:49], s[42:43], 18
	s_add_u32 s48, s21, s48
	s_addc_u32 s49, s22, s49
	s_ashr_i32 s41, s40, 31
	s_lshl_b64 s[50:51], s[40:41], 18
	s_add_u32 s50, s15, s50
	s_addc_u32 s51, s20, s51
	s_andn2_b64 vcc, exec, s[30:31]
	s_cbranch_vccnz .LBB0_336
	s_and_b64 s[60:61], s[46:47], exec
	s_cselect_b32 s39, s49, s55
	s_cselect_b32 s41, s48, s54
	s_cselect_b32 s43, s51, s59
	s_cselect_b32 s53, s50, s58
	s_add_u32 s69, s58, 0x100
	s_addc_u32 s70, s59, 0
	s_add_u32 s54, s54, 0x20080
	v_mov_b32_e32 v1, 0x3ecc95a3
	s_addc_u32 s55, s55, 0
	s_mov_b32 s58, 0
.Lpeelph1f_0:
	s_add_i32 s71, s58, 2
	s_add_u32 s59, s54, 0xfffe0080
	s_addc_u32 s60, s55, -1
	s_add_i32 s72, 0, 0x10000
	s_cmp_eq_u32 s65, s58
	s_cselect_b32 s61, s39, s60
	s_cselect_b32 s60, s41, s59
	s_cselect_b32 s59, s43, s70
	s_cselect_b32 s58, s53, s69
	s_add_i32 s73, 0, 0x14000
	v_add_u32_e32 v2, s72, v198
	v_add_u32_e32 v6, s73, v198
	ds_read_b128 v[26:29], v2
	ds_read_b128 v[30:33], v2 offset:1024
	ds_read_b128 v[18:21], v2 offset:2048
	ds_read_b128 v[22:25], v2 offset:3072
	ds_read_b128 v[10:13], v6
	ds_read_b128 v[14:17], v6 offset:1024
	ds_read_b128 v[2:5], v6 offset:2048
	ds_read_b128 v[6:9], v6 offset:3072
	v_lshl_add_u64 v[170:171], s[54:55], 0, v[186:187]
	s_add_i32 m0, s8, 0xc000
	ds_read_b128 v[188:191], v200
	ds_read_b128 v[192:195], v200 offset:1024
	ds_read_b128 v[202:205], v200 offset:2048
	ds_read_b128 v[206:209], v200 offset:3072
	ds_read_b128 v[210:213], v200 offset:4096
	ds_read_b128 v[214:217], v200 offset:5120
	ds_read_b128 v[236:239], v200 offset:6144
	ds_read_b128 v[240:243], v200 offset:7168
	global_load_lds_dwordx4 v[170:171], off
	v_lshl_add_u64 v[170:171], s[54:55], 0, v[184:185]
	s_add_i32 m0, s8, 0xe000
	s_nop 0
	global_load_lds_dwordx4 v[170:171], off
	s_waitcnt vmcnt(8)
	s_waitcnt lgkmcnt(0)
	s_barrier
	s_setprio 1
	s_waitcnt lgkmcnt(0)
	v_mfma_scale_f32_16x16x128_f8f6f4 v[158:161], v[26:33], v[188:195], 0, v196, v169 op_sel_hi:[0,0,0]
	v_mfma_scale_f32_16x16x128_f8f6f4 v[154:157], v[18:25], v[188:195], 0, v196, v169 op_sel_hi:[0,0,0]
	v_mfma_scale_f32_16x16x128_f8f6f4 v[142:145], v[26:33], v[202:209], 0, v196, v169 op_sel_hi:[0,0,0]
	v_mfma_scale_f32_16x16x128_f8f6f4 v[138:141], v[18:25], v[202:209], 0, v196, v169 op_sel_hi:[0,0,0]
	v_mfma_scale_f32_16x16x128_f8f6f4 v[126:129], v[26:33], v[210:217], 0, v196, v169 op_sel_hi:[0,0,0]
	v_mfma_scale_f32_16x16x128_f8f6f4 v[122:125], v[18:25], v[210:217], 0, v196, v169 op_sel_hi:[0,0,0]
	v_mfma_scale_f32_16x16x128_f8f6f4 v[110:113], v[26:33], v[236:243], 0, v196, v169 op_sel_hi:[0,0,0]
	v_mfma_scale_f32_16x16x128_f8f6f4 v[106:109], v[18:25], v[236:243], 0, v196, v169 op_sel_hi:[0,0,0]
	s_setprio 0
	s_setprio 1
	v_mfma_scale_f32_16x16x128_f8f6f4 v[150:153], v[10:17], v[188:195], 0, v196, v169 op_sel_hi:[0,0,0]
	v_mfma_scale_f32_16x16x128_f8f6f4 v[146:149], v[2:9], v[188:195], 0, v196, v169 op_sel_hi:[0,0,0]
	v_mfma_scale_f32_16x16x128_f8f6f4 v[134:137], v[10:17], v[202:209], 0, v196, v169 op_sel_hi:[0,0,0]
	v_mfma_scale_f32_16x16x128_f8f6f4 v[130:133], v[2:9], v[202:209], 0, v196, v169 op_sel_hi:[0,0,0]
	v_mfma_scale_f32_16x16x128_f8f6f4 v[118:121], v[10:17], v[210:217], 0, v196, v169 op_sel_hi:[0,0,0]
	v_mfma_scale_f32_16x16x128_f8f6f4 v[114:117], v[2:9], v[210:217], 0, v196, v169 op_sel_hi:[0,0,0]
	v_mfma_scale_f32_16x16x128_f8f6f4 v[102:105], v[10:17], v[236:243], 0, v196, v169 op_sel_hi:[0,0,0]
	v_mfma_scale_f32_16x16x128_f8f6f4 v[98:101], v[2:9], v[236:243], 0, v196, v169 op_sel_hi:[0,0,0]
	s_setprio 0
	s_barrier
	s_add_i32 s72, s72, s1
	v_lshl_add_u64 v[188:189], s[58:59], 0, v[162:163]
	s_mov_b32 m0, s72
	ds_read_b128 v[202:205], v200 offset:16384
	ds_read_b128 v[206:209], v200 offset:17408
	ds_read_b128 v[210:213], v200 offset:18432
	ds_read_b128 v[214:217], v200 offset:19456
	ds_read_b128 v[236:239], v200 offset:20480
	ds_read_b128 v[240:243], v200 offset:21504
	ds_read_b128 v[244:247], v200 offset:22528
	ds_read_b128 v[248:251], v200 offset:23552
	global_load_lds_dwordx4 v[188:189], off
	s_add_i32 m0, s72, 0x2000
	s_add_u32 s74, s58, 0x20000
	v_lshl_add_u64 v[190:191], s[58:59], 0, v[164:165]
	s_addc_u32 s75, s59, 0
	s_add_i32 s72, s73, s1
	global_load_lds_dwordx4 v[190:191], off
	v_lshl_add_u64 v[170:171], s[74:75], 0, v[162:163]
	s_mov_b32 m0, s72
	v_lshl_add_u64 v[192:193], s[60:61], 0, v[178:179]
	global_load_lds_dwordx4 v[170:171], off
	v_lshl_add_u64 v[170:171], s[74:75], 0, v[164:165]
	s_add_i32 m0, s72, 0x2000
	v_lshl_add_u64 v[194:195], s[60:61], 0, v[180:181]
	global_load_lds_dwordx4 v[170:171], off
	s_mov_b32 m0, s8
	s_nop 0
	global_load_lds_dwordx4 v[192:193], off
	s_mov_b32 m0, s11
	s_nop 0
	global_load_lds_dwordx4 v[194:195], off
	s_waitcnt vmcnt(8)
	s_waitcnt lgkmcnt(0)
	s_barrier
	s_setprio 1
	s_waitcnt lgkmcnt(0)
	v_mfma_scale_f32_16x16x128_f8f6f4 v[94:97], v[26:33], v[202:209], 0, v196, v169 op_sel_hi:[0,0,0]
	v_mfma_scale_f32_16x16x128_f8f6f4 v[90:93], v[18:25], v[202:209], 0, v196, v169 op_sel_hi:[0,0,0]
	v_mfma_scale_f32_16x16x128_f8f6f4 v[78:81], v[26:33], v[210:217], 0, v196, v169 op_sel_hi:[0,0,0]
	v_mfma_scale_f32_16x16x128_f8f6f4 v[74:77], v[18:25], v[210:217], 0, v196, v169 op_sel_hi:[0,0,0]
	v_mfma_scale_f32_16x16x128_f8f6f4 v[62:65], v[26:33], v[236:243], 0, v196, v169 op_sel_hi:[0,0,0]
	v_mfma_scale_f32_16x16x128_f8f6f4 v[58:61], v[18:25], v[236:243], 0, v196, v169 op_sel_hi:[0,0,0]
	v_mfma_scale_f32_16x16x128_f8f6f4 v[46:49], v[26:33], v[244:251], 0, v196, v169 op_sel_hi:[0,0,0]
	v_mfma_scale_f32_16x16x128_f8f6f4 v[42:45], v[18:25], v[244:251], 0, v196, v169 op_sel_hi:[0,0,0]
	s_setprio 0
	s_setprio 1
	v_mfma_scale_f32_16x16x128_f8f6f4 v[86:89], v[10:17], v[202:209], 0, v196, v169 op_sel_hi:[0,0,0]
	v_mfma_scale_f32_16x16x128_f8f6f4 v[82:85], v[2:9], v[202:209], 0, v196, v169 op_sel_hi:[0,0,0]
	v_mfma_scale_f32_16x16x128_f8f6f4 v[70:73], v[10:17], v[210:217], 0, v196, v169 op_sel_hi:[0,0,0]
	v_mfma_scale_f32_16x16x128_f8f6f4 v[66:69], v[2:9], v[210:217], 0, v196, v169 op_sel_hi:[0,0,0]
	v_mfma_scale_f32_16x16x128_f8f6f4 v[54:57], v[10:17], v[236:243], 0, v196, v169 op_sel_hi:[0,0,0]
	v_mfma_scale_f32_16x16x128_f8f6f4 v[50:53], v[2:9], v[236:243], 0, v196, v169 op_sel_hi:[0,0,0]
	v_mfma_scale_f32_16x16x128_f8f6f4 v[38:41], v[10:17], v[244:251], 0, v196, v169 op_sel_hi:[0,0,0]
	v_mfma_scale_f32_16x16x128_f8f6f4 v[34:37], v[2:9], v[244:251], 0, v196, v169 op_sel_hi:[0,0,0]
	s_setprio 0
	s_barrier
	s_add_i32 s72, 0, 0x18000
	s_add_i32 s73, 0, 0x1c000
	v_add_u32_e32 v2, s72, v198
	v_add_u32_e32 v6, s73, v198
	ds_read_b128 v[26:29], v2
	ds_read_b128 v[30:33], v2 offset:1024
	ds_read_b128 v[18:21], v2 offset:2048
	ds_read_b128 v[22:25], v2 offset:3072
	ds_read_b128 v[10:13], v6
	ds_read_b128 v[14:17], v6 offset:1024
	ds_read_b128 v[2:5], v6 offset:2048
	ds_read_b128 v[6:9], v6 offset:3072
	s_add_u32 s60, s60, 0x20000
	s_addc_u32 s61, s61, 0
	s_mov_b32 m0, s16
	v_lshl_add_u64 v[170:171], s[60:61], 0, v[178:179]
	ds_read_b128 v[202:205], v200 offset:32768
	ds_read_b128 v[206:209], v200 offset:33792
	ds_read_b128 v[210:213], v200 offset:34816
	ds_read_b128 v[214:217], v200 offset:35840
	ds_read_b128 v[236:239], v200 offset:36864
	ds_read_b128 v[240:243], v200 offset:37888
	ds_read_b128 v[244:247], v200 offset:38912
	ds_read_b128 v[248:251], v200 offset:39936
	global_load_lds_dwordx4 v[170:171], off
	v_lshl_add_u64 v[170:171], s[60:61], 0, v[180:181]
	s_mov_b32 m0, s25
	s_nop 0
	global_load_lds_dwordx4 v[170:171], off
	s_waitcnt vmcnt(8)
	s_waitcnt lgkmcnt(0)
	s_barrier
	s_setprio 1
	s_waitcnt lgkmcnt(0)
	v_mfma_scale_f32_16x16x128_f8f6f4 v[158:161], v[26:33], v[202:209], v[158:161], v196, v169 op_sel_hi:[0,0,0]
	v_mfma_scale_f32_16x16x128_f8f6f4 v[154:157], v[18:25], v[202:209], v[154:157], v196, v169 op_sel_hi:[0,0,0]
	v_mfma_scale_f32_16x16x128_f8f6f4 v[142:145], v[26:33], v[210:217], v[142:145], v196, v169 op_sel_hi:[0,0,0]
	v_mfma_scale_f32_16x16x128_f8f6f4 v[138:141], v[18:25], v[210:217], v[138:141], v196, v169 op_sel_hi:[0,0,0]
	v_mfma_scale_f32_16x16x128_f8f6f4 v[126:129], v[26:33], v[236:243], v[126:129], v196, v169 op_sel_hi:[0,0,0]
	v_mfma_scale_f32_16x16x128_f8f6f4 v[122:125], v[18:25], v[236:243], v[122:125], v196, v169 op_sel_hi:[0,0,0]
	v_mfma_scale_f32_16x16x128_f8f6f4 v[110:113], v[26:33], v[244:251], v[110:113], v196, v169 op_sel_hi:[0,0,0]
	v_mfma_scale_f32_16x16x128_f8f6f4 v[106:109], v[18:25], v[244:251], v[106:109], v196, v169 op_sel_hi:[0,0,0]
	s_setprio 0
	s_setprio 1
	v_mfma_scale_f32_16x16x128_f8f6f4 v[150:153], v[10:17], v[202:209], v[150:153], v196, v169 op_sel_hi:[0,0,0]
	v_mfma_scale_f32_16x16x128_f8f6f4 v[146:149], v[2:9], v[202:209], v[146:149], v196, v169 op_sel_hi:[0,0,0]
	v_mfma_scale_f32_16x16x128_f8f6f4 v[134:137], v[10:17], v[210:217], v[134:137], v196, v169 op_sel_hi:[0,0,0]
	v_mfma_scale_f32_16x16x128_f8f6f4 v[130:133], v[2:9], v[210:217], v[130:133], v196, v169 op_sel_hi:[0,0,0]
	v_mfma_scale_f32_16x16x128_f8f6f4 v[118:121], v[10:17], v[236:243], v[118:121], v196, v169 op_sel_hi:[0,0,0]
	v_mfma_scale_f32_16x16x128_f8f6f4 v[114:117], v[2:9], v[236:243], v[114:117], v196, v169 op_sel_hi:[0,0,0]
	v_mfma_scale_f32_16x16x128_f8f6f4 v[102:105], v[10:17], v[244:251], v[102:105], v196, v169 op_sel_hi:[0,0,0]
	v_mfma_scale_f32_16x16x128_f8f6f4 v[98:101], v[2:9], v[244:251], v[98:101], v196, v169 op_sel_hi:[0,0,0]
	s_setprio 0
	s_barrier
	s_add_i32 s60, s72, s1
	v_lshl_add_u64 v[170:171], v[188:189], 0, s[56:57]
	s_mov_b32 m0, s60
	ds_read_b128 v[202:205], v200 offset:49152
	ds_read_b128 v[206:209], v200 offset:50176
	ds_read_b128 v[210:213], v200 offset:51200
	ds_read_b128 v[214:217], v200 offset:52224
	ds_read_b128 v[236:239], v200 offset:53248
	ds_read_b128 v[240:243], v200 offset:54272
	ds_read_b128 v[244:247], v200 offset:55296
	ds_read_b128 v[248:251], v200 offset:56320
	global_load_lds_dwordx4 v[170:171], off
	s_add_i32 m0, s60, 0x2000
	s_add_u32 s58, s58, 0x20080
	v_lshl_add_u64 v[170:171], v[190:191], 0, s[56:57]
	s_addc_u32 s59, s59, 0
	s_add_i32 s60, s73, s1
	global_load_lds_dwordx4 v[170:171], off
	v_lshl_add_u64 v[170:171], s[58:59], 0, v[162:163]
	s_mov_b32 m0, s60
	s_nop 0
	global_load_lds_dwordx4 v[170:171], off
	v_lshl_add_u64 v[170:171], s[58:59], 0, v[164:165]
	s_add_i32 m0, s60, 0x2000
	s_nop 0
	global_load_lds_dwordx4 v[170:171], off
	v_lshl_add_u64 v[170:171], v[192:193], 0, s[56:57]
	s_mov_b32 m0, s62
	s_nop 0
	global_load_lds_dwordx4 v[170:171], off
	v_lshl_add_u64 v[170:171], v[194:195], 0, s[56:57]
	s_mov_b32 m0, s63
	s_nop 0
	global_load_lds_dwordx4 v[170:171], off
	s_waitcnt vmcnt(8)
	s_waitcnt lgkmcnt(0)
	s_barrier
	s_setprio 1
	s_waitcnt lgkmcnt(0)
	v_mfma_scale_f32_16x16x128_f8f6f4 v[94:97], v[26:33], v[202:209], v[94:97], v196, v169 op_sel_hi:[0,0,0]
	v_mfma_scale_f32_16x16x128_f8f6f4 v[90:93], v[18:25], v[202:209], v[90:93], v196, v169 op_sel_hi:[0,0,0]
	v_mfma_scale_f32_16x16x128_f8f6f4 v[78:81], v[26:33], v[210:217], v[78:81], v196, v169 op_sel_hi:[0,0,0]
	v_mfma_scale_f32_16x16x128_f8f6f4 v[74:77], v[18:25], v[210:217], v[74:77], v196, v169 op_sel_hi:[0,0,0]
	v_mfma_scale_f32_16x16x128_f8f6f4 v[62:65], v[26:33], v[236:243], v[62:65], v196, v169 op_sel_hi:[0,0,0]
	v_mfma_scale_f32_16x16x128_f8f6f4 v[58:61], v[18:25], v[236:243], v[58:61], v196, v169 op_sel_hi:[0,0,0]
	v_mfma_scale_f32_16x16x128_f8f6f4 v[46:49], v[26:33], v[244:251], v[46:49], v196, v169 op_sel_hi:[0,0,0]
	v_mfma_scale_f32_16x16x128_f8f6f4 v[42:45], v[18:25], v[244:251], v[42:45], v196, v169 op_sel_hi:[0,0,0]
	s_setprio 0
	s_setprio 1
	v_mfma_scale_f32_16x16x128_f8f6f4 v[86:89], v[10:17], v[202:209], v[86:89], v196, v169 op_sel_hi:[0,0,0]
	v_mfma_scale_f32_16x16x128_f8f6f4 v[82:85], v[2:9], v[202:209], v[82:85], v196, v169 op_sel_hi:[0,0,0]
	v_mfma_scale_f32_16x16x128_f8f6f4 v[70:73], v[10:17], v[210:217], v[70:73], v196, v169 op_sel_hi:[0,0,0]
	v_mfma_scale_f32_16x16x128_f8f6f4 v[66:69], v[2:9], v[210:217], v[66:69], v196, v169 op_sel_hi:[0,0,0]
	v_mfma_scale_f32_16x16x128_f8f6f4 v[54:57], v[10:17], v[236:243], v[54:57], v196, v169 op_sel_hi:[0,0,0]
	v_mfma_scale_f32_16x16x128_f8f6f4 v[50:53], v[2:9], v[236:243], v[50:53], v196, v169 op_sel_hi:[0,0,0]
	v_mfma_scale_f32_16x16x128_f8f6f4 v[38:41], v[10:17], v[244:251], v[38:41], v196, v169 op_sel_hi:[0,0,0]
	v_mfma_scale_f32_16x16x128_f8f6f4 v[34:37], v[2:9], v[244:251], v[34:37], v196, v169 op_sel_hi:[0,0,0]
	s_setprio 0
	s_barrier
	s_add_u32 s69, s69, 0x100
	s_addc_u32 s70, s70, 0
	s_add_u32 s54, s54, 0x100
	s_addc_u32 s55, s55, 0
	s_cmp_ge_i32 s71, s0
	s_mov_b32 s58, s71
	s_cbranch_scc0 .LBB0_298
	s_branch .Lpeelexitph1f

.Lpeelexitph1f:
	s_mov_b64 s[72:73], 0xe800000
	s_mov_b64 s[70:71], 0xe800800
	v_mov_b32_e32 v209, v1
	s_and_b64 vcc, exec, s[34:35]
	s_cbranch_vccz .LBB0_301

.LBB0_467:
	s_lshl_b64 s[60:61], s[50:51], 16
	s_add_u32 s60, s11, s60
	s_addc_u32 s61, s12, s61
	s_andn2_b64 vcc, exec, s[40:41]
	s_cbranch_vccnz .LBB0_470
	s_and_b64 s[70:71], exec, s[54:55]
	s_cselect_b32 s51, s61, s69
	s_cselect_b32 s53, s60, s68
	s_add_u32 s66, s68, 0x100
	s_addc_u32 s72, s69, 0
	s_add_u32 s64, s64, 0x40080
	s_addc_u32 s65, s65, 0
	s_mov_b32 s68, 0
.Lpeelph3_0:
	s_add_i32 s73, s68, 2
	s_add_u32 s69, s64, 0xfffc0080
	s_addc_u32 s70, s65, -1
	s_add_i32 s74, 0, 0x10000
	s_cmp_eq_u32 s24, s68
	s_cselect_b32 s71, s59, s70
	s_cselect_b32 s70, s58, s69
	s_cselect_b32 s69, s51, s72
	s_cselect_b32 s68, s53, s66
	s_add_i32 s76, 0, 0x14000
	v_add_u32_e32 v152, s74, v220
	v_add_u32_e32 v164, s76, v220
	ds_read_b128 v[106:109], v152
	ds_read_b128 v[110:113], v152 offset:1024
	ds_read_b128 v[114:117], v152 offset:2048
	ds_read_b128 v[152:155], v152 offset:3072
	ds_read_b128 v[156:159], v164
	ds_read_b128 v[160:163], v164 offset:1024
	ds_read_b128 v[170:173], v164 offset:2048
	ds_read_b128 v[174:177], v164 offset:3072
	v_lshl_add_u64 v[164:165], s[64:65], 0, v[150:151]
	s_add_i32 m0, s14, 0xc000
	ds_read_b128 v[178:181], v222
	ds_read_b128 v[182:185], v222 offset:1024
	ds_read_b128 v[186:189], v222 offset:2048
	ds_read_b128 v[190:193], v222 offset:3072
	ds_read_b128 v[194:197], v222 offset:4096
	ds_read_b128 v[198:201], v222 offset:5120
	ds_read_b128 v[202:205], v222 offset:6144
	ds_read_b128 v[206:209], v222 offset:7168
	global_load_lds_dwordx4 v[164:165], off
	v_lshl_add_u64 v[164:165], s[64:65], 0, v[148:149]
	s_add_i32 m0, s14, 0xe000
	s_nop 0
	global_load_lds_dwordx4 v[164:165], off
	s_waitcnt vmcnt(8)
	s_waitcnt lgkmcnt(0)
	s_barrier
	s_setprio 1
	s_waitcnt lgkmcnt(0)
	v_mfma_f32_16x16x32_bf16 v[138:141], v[106:109], v[178:181], 0
	v_mfma_f32_16x16x32_bf16 v[62:65], v[114:117], v[178:181], 0
	v_mfma_f32_16x16x32_bf16 v[130:133], v[106:109], v[186:189], 0
	v_mfma_f32_16x16x32_bf16 v[54:57], v[114:117], v[186:189], 0
	v_mfma_f32_16x16x32_bf16 v[122:125], v[106:109], v[194:197], 0
	v_mfma_f32_16x16x32_bf16 v[46:49], v[114:117], v[194:197], 0
	v_mfma_f32_16x16x32_bf16 v[102:105], v[106:109], v[202:205], 0
	v_mfma_f32_16x16x32_bf16 v[38:41], v[114:117], v[202:205], 0
	v_mfma_f32_16x16x32_bf16 v[138:141], v[110:113], v[182:185], v[138:141]
	v_mfma_f32_16x16x32_bf16 v[62:65], v[152:155], v[182:185], v[62:65]
	v_mfma_f32_16x16x32_bf16 v[130:133], v[110:113], v[190:193], v[130:133]
	v_mfma_f32_16x16x32_bf16 v[54:57], v[152:155], v[190:193], v[54:57]
	v_mfma_f32_16x16x32_bf16 v[122:125], v[110:113], v[198:201], v[122:125]
	v_mfma_f32_16x16x32_bf16 v[46:49], v[152:155], v[198:201], v[46:49]
	v_mfma_f32_16x16x32_bf16 v[102:105], v[110:113], v[206:209], v[102:105]
	v_mfma_f32_16x16x32_bf16 v[38:41], v[152:155], v[206:209], v[38:41]
	s_setprio 0
	s_setprio 1
	v_mfma_f32_16x16x32_bf16 v[134:137], v[156:159], v[178:181], 0
	v_mfma_f32_16x16x32_bf16 v[58:61], v[170:173], v[178:181], 0
	v_mfma_f32_16x16x32_bf16 v[126:129], v[156:159], v[186:189], 0
	v_mfma_f32_16x16x32_bf16 v[50:53], v[170:173], v[186:189], 0
	v_mfma_f32_16x16x32_bf16 v[118:121], v[156:159], v[194:197], 0
	v_mfma_f32_16x16x32_bf16 v[42:45], v[170:173], v[194:197], 0
	v_mfma_f32_16x16x32_bf16 v[98:101], v[156:159], v[202:205], 0
	v_mfma_f32_16x16x32_bf16 v[34:37], v[170:173], v[202:205], 0
	v_mfma_f32_16x16x32_bf16 v[134:137], v[160:163], v[182:185], v[134:137]
	v_mfma_f32_16x16x32_bf16 v[58:61], v[174:177], v[182:185], v[58:61]
	v_mfma_f32_16x16x32_bf16 v[126:129], v[160:163], v[190:193], v[126:129]
	v_mfma_f32_16x16x32_bf16 v[50:53], v[174:177], v[190:193], v[50:53]
	v_mfma_f32_16x16x32_bf16 v[118:121], v[160:163], v[198:201], v[118:121]
	v_mfma_f32_16x16x32_bf16 v[42:45], v[174:177], v[198:201], v[42:45]
	v_mfma_f32_16x16x32_bf16 v[98:101], v[160:163], v[206:209], v[98:101]
	v_mfma_f32_16x16x32_bf16 v[34:37], v[174:177], v[206:209], v[34:37]
	s_setprio 0
	s_barrier
	s_add_i32 s74, s74, s13
	v_lshl_add_u64 v[164:165], s[68:69], 0, v[166:167]
	s_mov_b32 m0, s74
	ds_read_b128 v[178:181], v222 offset:16384
	ds_read_b128 v[182:185], v222 offset:17408
	ds_read_b128 v[186:189], v222 offset:18432
	ds_read_b128 v[190:193], v222 offset:19456
	ds_read_b128 v[194:197], v222 offset:20480
	ds_read_b128 v[198:201], v222 offset:21504
	ds_read_b128 v[202:205], v222 offset:22528
	ds_read_b128 v[206:209], v222 offset:23552
	global_load_lds_dwordx4 v[164:165], off
	s_add_i32 m0, s74, 0x2000
	s_add_u32 s74, s68, 0x8000
	v_lshl_add_u64 v[210:211], s[68:69], 0, v[142:143]
	s_addc_u32 s75, s69, 0
	s_add_i32 s76, s76, s13
	global_load_lds_dwordx4 v[210:211], off
	v_lshl_add_u64 v[212:213], s[74:75], 0, v[166:167]
	s_mov_b32 m0, s76
	v_lshl_add_u64 v[214:215], s[70:71], 0, v[146:147]
	global_load_lds_dwordx4 v[212:213], off
	v_lshl_add_u64 v[212:213], s[74:75], 0, v[142:143]
	s_add_i32 m0, s76, 0x2000
	s_nop 0
	global_load_lds_dwordx4 v[212:213], off
	v_lshl_add_u64 v[212:213], s[70:71], 0, v[144:145]
	s_mov_b32 m0, s14
	s_nop 0
	global_load_lds_dwordx4 v[212:213], off
	s_mov_b32 m0, s15
	s_nop 0
	global_load_lds_dwordx4 v[214:215], off
	s_waitcnt vmcnt(8)
	s_waitcnt lgkmcnt(0)
	s_barrier
	s_setprio 1
	s_waitcnt lgkmcnt(0)
	v_mfma_f32_16x16x32_bf16 v[94:97], v[106:109], v[178:181], 0
	v_mfma_f32_16x16x32_bf16 v[30:33], v[114:117], v[178:181], 0
	v_mfma_f32_16x16x32_bf16 v[86:89], v[106:109], v[186:189], 0
	v_mfma_f32_16x16x32_bf16 v[22:25], v[114:117], v[186:189], 0
	v_mfma_f32_16x16x32_bf16 v[78:81], v[106:109], v[194:197], 0
	v_mfma_f32_16x16x32_bf16 v[14:17], v[114:117], v[194:197], 0
	v_mfma_f32_16x16x32_bf16 v[70:73], v[106:109], v[202:205], 0
	v_mfma_f32_16x16x32_bf16 v[6:9], v[114:117], v[202:205], 0
	v_mfma_f32_16x16x32_bf16 v[94:97], v[110:113], v[182:185], v[94:97]
	v_mfma_f32_16x16x32_bf16 v[30:33], v[152:155], v[182:185], v[30:33]
	v_mfma_f32_16x16x32_bf16 v[86:89], v[110:113], v[190:193], v[86:89]
	v_mfma_f32_16x16x32_bf16 v[22:25], v[152:155], v[190:193], v[22:25]
	v_mfma_f32_16x16x32_bf16 v[78:81], v[110:113], v[198:201], v[78:81]
	v_mfma_f32_16x16x32_bf16 v[14:17], v[152:155], v[198:201], v[14:17]
	v_mfma_f32_16x16x32_bf16 v[70:73], v[110:113], v[206:209], v[70:73]
	v_mfma_f32_16x16x32_bf16 v[6:9], v[152:155], v[206:209], v[6:9]
	s_setprio 0
	s_setprio 1
	v_mfma_f32_16x16x32_bf16 v[90:93], v[156:159], v[178:181], 0
	v_mfma_f32_16x16x32_bf16 v[26:29], v[170:173], v[178:181], 0
	v_mfma_f32_16x16x32_bf16 v[82:85], v[156:159], v[186:189], 0
	v_mfma_f32_16x16x32_bf16 v[18:21], v[170:173], v[186:189], 0
	v_mfma_f32_16x16x32_bf16 v[74:77], v[156:159], v[194:197], 0
	v_mfma_f32_16x16x32_bf16 v[10:13], v[170:173], v[194:197], 0
	v_mfma_f32_16x16x32_bf16 v[66:69], v[156:159], v[202:205], 0
	v_mfma_f32_16x16x32_bf16 v[2:5], v[170:173], v[202:205], 0
	v_mfma_f32_16x16x32_bf16 v[90:93], v[160:163], v[182:185], v[90:93]
	v_mfma_f32_16x16x32_bf16 v[26:29], v[174:177], v[182:185], v[26:29]
	v_mfma_f32_16x16x32_bf16 v[82:85], v[160:163], v[190:193], v[82:85]
	v_mfma_f32_16x16x32_bf16 v[18:21], v[174:177], v[190:193], v[18:21]
	v_mfma_f32_16x16x32_bf16 v[74:77], v[160:163], v[198:201], v[74:77]
	v_mfma_f32_16x16x32_bf16 v[10:13], v[174:177], v[198:201], v[10:13]
	v_mfma_f32_16x16x32_bf16 v[66:69], v[160:163], v[206:209], v[66:69]
	v_mfma_f32_16x16x32_bf16 v[2:5], v[174:177], v[206:209], v[2:5]
	s_setprio 0
	s_barrier
	s_add_i32 s74, 0, 0x18000
	s_add_i32 s75, 0, 0x1c000
	v_add_u32_e32 v152, s74, v220
	v_add_u32_e32 v174, s75, v220
	ds_read_b128 v[106:109], v152
	ds_read_b128 v[110:113], v152 offset:1024
	ds_read_b128 v[114:117], v152 offset:2048
	ds_read_b128 v[152:155], v152 offset:3072
	ds_read_b128 v[156:159], v174
	ds_read_b128 v[160:163], v174 offset:1024
	ds_read_b128 v[170:173], v174 offset:2048
	ds_read_b128 v[174:177], v174 offset:3072
	s_add_u32 s70, s70, 0x40000
	s_addc_u32 s71, s71, 0
	s_mov_b32 m0, s16
	v_lshl_add_u64 v[216:217], s[70:71], 0, v[144:145]
	ds_read_b128 v[178:181], v222 offset:32768
	ds_read_b128 v[182:185], v222 offset:33792
	ds_read_b128 v[186:189], v222 offset:34816
	ds_read_b128 v[190:193], v222 offset:35840
	ds_read_b128 v[194:197], v222 offset:36864
	ds_read_b128 v[198:201], v222 offset:37888
	ds_read_b128 v[202:205], v222 offset:38912
	ds_read_b128 v[206:209], v222 offset:39936
	global_load_lds_dwordx4 v[216:217], off
	v_lshl_add_u64 v[216:217], s[70:71], 0, v[146:147]
	s_mov_b32 m0, s20
	s_nop 0
	global_load_lds_dwordx4 v[216:217], off
	s_waitcnt vmcnt(8)
	s_waitcnt lgkmcnt(0)
	s_barrier
	s_setprio 1
	s_waitcnt lgkmcnt(0)
	v_mfma_f32_16x16x32_bf16 v[138:141], v[106:109], v[178:181], v[138:141]
	v_mfma_f32_16x16x32_bf16 v[62:65], v[114:117], v[178:181], v[62:65]
	v_mfma_f32_16x16x32_bf16 v[130:133], v[106:109], v[186:189], v[130:133]
	v_mfma_f32_16x16x32_bf16 v[54:57], v[114:117], v[186:189], v[54:57]
	v_mfma_f32_16x16x32_bf16 v[122:125], v[106:109], v[194:197], v[122:125]
	v_mfma_f32_16x16x32_bf16 v[46:49], v[114:117], v[194:197], v[46:49]
	v_mfma_f32_16x16x32_bf16 v[102:105], v[106:109], v[202:205], v[102:105]
	v_mfma_f32_16x16x32_bf16 v[38:41], v[114:117], v[202:205], v[38:41]
	v_mfma_f32_16x16x32_bf16 v[138:141], v[110:113], v[182:185], v[138:141]
	v_mfma_f32_16x16x32_bf16 v[62:65], v[152:155], v[182:185], v[62:65]
	v_mfma_f32_16x16x32_bf16 v[130:133], v[110:113], v[190:193], v[130:133]
	v_mfma_f32_16x16x32_bf16 v[54:57], v[152:155], v[190:193], v[54:57]
	v_mfma_f32_16x16x32_bf16 v[122:125], v[110:113], v[198:201], v[122:125]
	v_mfma_f32_16x16x32_bf16 v[46:49], v[152:155], v[198:201], v[46:49]
	v_mfma_f32_16x16x32_bf16 v[102:105], v[110:113], v[206:209], v[102:105]
	v_mfma_f32_16x16x32_bf16 v[38:41], v[152:155], v[206:209], v[38:41]
	s_setprio 0
	s_setprio 1
	v_mfma_f32_16x16x32_bf16 v[134:137], v[156:159], v[178:181], v[134:137]
	v_mfma_f32_16x16x32_bf16 v[58:61], v[170:173], v[178:181], v[58:61]
	v_mfma_f32_16x16x32_bf16 v[126:129], v[156:159], v[186:189], v[126:129]
	v_mfma_f32_16x16x32_bf16 v[50:53], v[170:173], v[186:189], v[50:53]
	v_mfma_f32_16x16x32_bf16 v[118:121], v[156:159], v[194:197], v[118:121]
	v_mfma_f32_16x16x32_bf16 v[42:45], v[170:173], v[194:197], v[42:45]
	v_mfma_f32_16x16x32_bf16 v[98:101], v[156:159], v[202:205], v[98:101]
	v_mfma_f32_16x16x32_bf16 v[34:37], v[170:173], v[202:205], v[34:37]
	v_mfma_f32_16x16x32_bf16 v[134:137], v[160:163], v[182:185], v[134:137]
	v_mfma_f32_16x16x32_bf16 v[58:61], v[174:177], v[182:185], v[58:61]
	v_mfma_f32_16x16x32_bf16 v[126:129], v[160:163], v[190:193], v[126:129]
	v_mfma_f32_16x16x32_bf16 v[50:53], v[174:177], v[190:193], v[50:53]
	v_mfma_f32_16x16x32_bf16 v[118:121], v[160:163], v[198:201], v[118:121]
	v_mfma_f32_16x16x32_bf16 v[42:45], v[174:177], v[198:201], v[42:45]
	v_mfma_f32_16x16x32_bf16 v[98:101], v[160:163], v[206:209], v[98:101]
	v_mfma_f32_16x16x32_bf16 v[34:37], v[174:177], v[206:209], v[34:37]
	s_setprio 0
	s_barrier
	s_add_i32 s70, s74, s13
	v_lshl_add_u64 v[164:165], v[164:165], 0, s[56:57]
	s_mov_b32 m0, s70
	ds_read_b128 v[178:181], v222 offset:49152
	ds_read_b128 v[182:185], v222 offset:50176
	ds_read_b128 v[186:189], v222 offset:51200
	ds_read_b128 v[190:193], v222 offset:52224
	ds_read_b128 v[194:197], v222 offset:53248
	ds_read_b128 v[198:201], v222 offset:54272
	ds_read_b128 v[202:205], v222 offset:55296
	ds_read_b128 v[206:209], v222 offset:56320
	global_load_lds_dwordx4 v[164:165], off
	s_add_i32 m0, s70, 0x2000
	s_add_u32 s68, s68, 0x8080
	v_lshl_add_u64 v[164:165], v[210:211], 0, s[56:57]
	s_addc_u32 s69, s69, 0
	s_add_i32 s70, s75, s13
	global_load_lds_dwordx4 v[164:165], off
	v_lshl_add_u64 v[164:165], s[68:69], 0, v[166:167]
	s_mov_b32 m0, s70
	s_nop 0
	global_load_lds_dwordx4 v[164:165], off
	v_lshl_add_u64 v[164:165], s[68:69], 0, v[142:143]
	s_add_i32 m0, s70, 0x2000
	s_nop 0
	global_load_lds_dwordx4 v[164:165], off
	v_lshl_add_u64 v[164:165], v[212:213], 0, s[56:57]
	s_mov_b32 m0, s21
	s_nop 0
	global_load_lds_dwordx4 v[164:165], off
	v_lshl_add_u64 v[164:165], v[214:215], 0, s[56:57]
	s_mov_b32 m0, s22
	s_nop 0
	global_load_lds_dwordx4 v[164:165], off
	s_waitcnt vmcnt(8)
	s_waitcnt lgkmcnt(0)
	s_barrier
	s_setprio 1
	s_waitcnt lgkmcnt(0)
	v_mfma_f32_16x16x32_bf16 v[94:97], v[106:109], v[178:181], v[94:97]
	v_mfma_f32_16x16x32_bf16 v[30:33], v[114:117], v[178:181], v[30:33]
	v_mfma_f32_16x16x32_bf16 v[86:89], v[106:109], v[186:189], v[86:89]
	v_mfma_f32_16x16x32_bf16 v[22:25], v[114:117], v[186:189], v[22:25]
	v_mfma_f32_16x16x32_bf16 v[78:81], v[106:109], v[194:197], v[78:81]
	v_mfma_f32_16x16x32_bf16 v[14:17], v[114:117], v[194:197], v[14:17]
	v_mfma_f32_16x16x32_bf16 v[70:73], v[106:109], v[202:205], v[70:73]
	v_mfma_f32_16x16x32_bf16 v[6:9], v[114:117], v[202:205], v[6:9]
	v_mfma_f32_16x16x32_bf16 v[94:97], v[110:113], v[182:185], v[94:97]
	v_mfma_f32_16x16x32_bf16 v[30:33], v[152:155], v[182:185], v[30:33]
	v_mfma_f32_16x16x32_bf16 v[86:89], v[110:113], v[190:193], v[86:89]
	v_mfma_f32_16x16x32_bf16 v[22:25], v[152:155], v[190:193], v[22:25]
	v_mfma_f32_16x16x32_bf16 v[78:81], v[110:113], v[198:201], v[78:81]
	v_mfma_f32_16x16x32_bf16 v[14:17], v[152:155], v[198:201], v[14:17]
	v_mfma_f32_16x16x32_bf16 v[70:73], v[110:113], v[206:209], v[70:73]
	v_mfma_f32_16x16x32_bf16 v[6:9], v[152:155], v[206:209], v[6:9]
	s_setprio 0
	s_setprio 1
	v_mfma_f32_16x16x32_bf16 v[90:93], v[156:159], v[178:181], v[90:93]
	v_mfma_f32_16x16x32_bf16 v[26:29], v[170:173], v[178:181], v[26:29]
	v_mfma_f32_16x16x32_bf16 v[82:85], v[156:159], v[186:189], v[82:85]
	v_mfma_f32_16x16x32_bf16 v[18:21], v[170:173], v[186:189], v[18:21]
	v_mfma_f32_16x16x32_bf16 v[74:77], v[156:159], v[194:197], v[74:77]
	v_mfma_f32_16x16x32_bf16 v[10:13], v[170:173], v[194:197], v[10:13]
	v_mfma_f32_16x16x32_bf16 v[66:69], v[156:159], v[202:205], v[66:69]
	v_mfma_f32_16x16x32_bf16 v[2:5], v[170:173], v[202:205], v[2:5]
	v_mfma_f32_16x16x32_bf16 v[90:93], v[160:163], v[182:185], v[90:93]
	v_mfma_f32_16x16x32_bf16 v[26:29], v[174:177], v[182:185], v[26:29]
	v_mfma_f32_16x16x32_bf16 v[82:85], v[160:163], v[190:193], v[82:85]
	v_mfma_f32_16x16x32_bf16 v[18:21], v[174:177], v[190:193], v[18:21]
	v_mfma_f32_16x16x32_bf16 v[74:77], v[160:163], v[198:201], v[74:77]
	v_mfma_f32_16x16x32_bf16 v[10:13], v[174:177], v[198:201], v[10:13]
	v_mfma_f32_16x16x32_bf16 v[66:69], v[160:163], v[206:209], v[66:69]
	v_mfma_f32_16x16x32_bf16 v[2:5], v[174:177], v[206:209], v[2:5]
	s_setprio 0
	s_barrier
	s_add_u32 s66, s66, 0x100
	s_addc_u32 s72, s72, 0
	s_add_u32 s64, s64, 0x100
	s_addc_u32 s65, s65, 0
	s_cmp_ge_i32 s73, s1
	s_mov_b32 s68, s73
	s_cbranch_scc0 .LBB0_469
	s_branch .Lpeelexitph3
.LBB0_469:
	s_add_i32 s73, s68, 2
	s_add_u32 s69, s64, 0xfffc0080
	s_addc_u32 s70, s65, -1
	s_add_i32 s74, 0, 0x10000
	s_cmp_eq_u32 s24, s68
	s_cselect_b32 s71, s59, s70
	s_cselect_b32 s70, s58, s69
	s_cselect_b32 s69, s51, s72
	s_cselect_b32 s68, s53, s66
	s_add_i32 s76, 0, 0x14000
	v_add_u32_e32 v152, s74, v220
	v_add_u32_e32 v164, s76, v220
	ds_read_b128 v[106:109], v152
	ds_read_b128 v[110:113], v152 offset:1024
	ds_read_b128 v[114:117], v152 offset:2048
	ds_read_b128 v[152:155], v152 offset:3072
	ds_read_b128 v[156:159], v164
	ds_read_b128 v[160:163], v164 offset:1024
	ds_read_b128 v[170:173], v164 offset:2048
	ds_read_b128 v[174:177], v164 offset:3072
	v_lshl_add_u64 v[164:165], s[64:65], 0, v[150:151]
	s_add_i32 m0, s14, 0xc000
	ds_read_b128 v[178:181], v222
	ds_read_b128 v[182:185], v222 offset:1024
	ds_read_b128 v[186:189], v222 offset:2048
	ds_read_b128 v[190:193], v222 offset:3072
	ds_read_b128 v[194:197], v222 offset:4096
	ds_read_b128 v[198:201], v222 offset:5120
	ds_read_b128 v[202:205], v222 offset:6144
	ds_read_b128 v[206:209], v222 offset:7168
	global_load_lds_dwordx4 v[164:165], off
	v_lshl_add_u64 v[164:165], s[64:65], 0, v[148:149]
	s_add_i32 m0, s14, 0xe000
	s_nop 0
	global_load_lds_dwordx4 v[164:165], off
	s_waitcnt vmcnt(8)
	s_waitcnt lgkmcnt(0)
	s_barrier
	s_setprio 1
	s_waitcnt lgkmcnt(0)
	v_mfma_f32_16x16x32_bf16 v[138:141], v[106:109], v[178:181], v[138:141]
	v_mfma_f32_16x16x32_bf16 v[62:65], v[114:117], v[178:181], v[62:65]
	v_mfma_f32_16x16x32_bf16 v[130:133], v[106:109], v[186:189], v[130:133]
	v_mfma_f32_16x16x32_bf16 v[54:57], v[114:117], v[186:189], v[54:57]
	v_mfma_f32_16x16x32_bf16 v[122:125], v[106:109], v[194:197], v[122:125]
	v_mfma_f32_16x16x32_bf16 v[46:49], v[114:117], v[194:197], v[46:49]
	v_mfma_f32_16x16x32_bf16 v[102:105], v[106:109], v[202:205], v[102:105]
	v_mfma_f32_16x16x32_bf16 v[38:41], v[114:117], v[202:205], v[38:41]
	v_mfma_f32_16x16x32_bf16 v[138:141], v[110:113], v[182:185], v[138:141]
	v_mfma_f32_16x16x32_bf16 v[62:65], v[152:155], v[182:185], v[62:65]
	v_mfma_f32_16x16x32_bf16 v[130:133], v[110:113], v[190:193], v[130:133]
	v_mfma_f32_16x16x32_bf16 v[54:57], v[152:155], v[190:193], v[54:57]
	v_mfma_f32_16x16x32_bf16 v[122:125], v[110:113], v[198:201], v[122:125]
	v_mfma_f32_16x16x32_bf16 v[46:49], v[152:155], v[198:201], v[46:49]
	v_mfma_f32_16x16x32_bf16 v[102:105], v[110:113], v[206:209], v[102:105]
	v_mfma_f32_16x16x32_bf16 v[38:41], v[152:155], v[206:209], v[38:41]
	s_setprio 0
	s_setprio 1
	v_mfma_f32_16x16x32_bf16 v[134:137], v[156:159], v[178:181], v[134:137]
	v_mfma_f32_16x16x32_bf16 v[58:61], v[170:173], v[178:181], v[58:61]
	v_mfma_f32_16x16x32_bf16 v[126:129], v[156:159], v[186:189], v[126:129]
	v_mfma_f32_16x16x32_bf16 v[50:53], v[170:173], v[186:189], v[50:53]
	v_mfma_f32_16x16x32_bf16 v[118:121], v[156:159], v[194:197], v[118:121]
	v_mfma_f32_16x16x32_bf16 v[42:45], v[170:173], v[194:197], v[42:45]
	v_mfma_f32_16x16x32_bf16 v[98:101], v[156:159], v[202:205], v[98:101]
	v_mfma_f32_16x16x32_bf16 v[34:37], v[170:173], v[202:205], v[34:37]
	v_mfma_f32_16x16x32_bf16 v[134:137], v[160:163], v[182:185], v[134:137]
	v_mfma_f32_16x16x32_bf16 v[58:61], v[174:177], v[182:185], v[58:61]
	v_mfma_f32_16x16x32_bf16 v[126:129], v[160:163], v[190:193], v[126:129]
	v_mfma_f32_16x16x32_bf16 v[50:53], v[174:177], v[190:193], v[50:53]
	v_mfma_f32_16x16x32_bf16 v[118:121], v[160:163], v[198:201], v[118:121]
	v_mfma_f32_16x16x32_bf16 v[42:45], v[174:177], v[198:201], v[42:45]
	v_mfma_f32_16x16x32_bf16 v[98:101], v[160:163], v[206:209], v[98:101]
	v_mfma_f32_16x16x32_bf16 v[34:37], v[174:177], v[206:209], v[34:37]
	s_setprio 0
	s_barrier
	s_add_i32 s74, s74, s13
	v_lshl_add_u64 v[164:165], s[68:69], 0, v[166:167]
	s_mov_b32 m0, s74
	ds_read_b128 v[178:181], v222 offset:16384
	ds_read_b128 v[182:185], v222 offset:17408
	ds_read_b128 v[186:189], v222 offset:18432
	ds_read_b128 v[190:193], v222 offset:19456
	ds_read_b128 v[194:197], v222 offset:20480
	ds_read_b128 v[198:201], v222 offset:21504
	ds_read_b128 v[202:205], v222 offset:22528
	ds_read_b128 v[206:209], v222 offset:23552
	global_load_lds_dwordx4 v[164:165], off
	s_add_i32 m0, s74, 0x2000
	s_add_u32 s74, s68, 0x8000
	v_lshl_add_u64 v[210:211], s[68:69], 0, v[142:143]
	s_addc_u32 s75, s69, 0
	s_add_i32 s76, s76, s13
	global_load_lds_dwordx4 v[210:211], off
	v_lshl_add_u64 v[212:213], s[74:75], 0, v[166:167]
	s_mov_b32 m0, s76
	v_lshl_add_u64 v[214:215], s[70:71], 0, v[146:147]
	global_load_lds_dwordx4 v[212:213], off
	v_lshl_add_u64 v[212:213], s[74:75], 0, v[142:143]
	s_add_i32 m0, s76, 0x2000
	s_nop 0
	global_load_lds_dwordx4 v[212:213], off
	v_lshl_add_u64 v[212:213], s[70:71], 0, v[144:145]
	s_mov_b32 m0, s14
	s_nop 0
	global_load_lds_dwordx4 v[212:213], off
	s_mov_b32 m0, s15
	s_nop 0
	global_load_lds_dwordx4 v[214:215], off
	s_waitcnt vmcnt(8)
	s_waitcnt lgkmcnt(0)
	s_barrier
	s_setprio 1
	s_waitcnt lgkmcnt(0)
	v_mfma_f32_16x16x32_bf16 v[94:97], v[106:109], v[178:181], v[94:97]
	v_mfma_f32_16x16x32_bf16 v[30:33], v[114:117], v[178:181], v[30:33]
	v_mfma_f32_16x16x32_bf16 v[86:89], v[106:109], v[186:189], v[86:89]
	v_mfma_f32_16x16x32_bf16 v[22:25], v[114:117], v[186:189], v[22:25]
	v_mfma_f32_16x16x32_bf16 v[78:81], v[106:109], v[194:197], v[78:81]
	v_mfma_f32_16x16x32_bf16 v[14:17], v[114:117], v[194:197], v[14:17]
	v_mfma_f32_16x16x32_bf16 v[70:73], v[106:109], v[202:205], v[70:73]
	v_mfma_f32_16x16x32_bf16 v[6:9], v[114:117], v[202:205], v[6:9]
	v_mfma_f32_16x16x32_bf16 v[94:97], v[110:113], v[182:185], v[94:97]
	v_mfma_f32_16x16x32_bf16 v[30:33], v[152:155], v[182:185], v[30:33]
	v_mfma_f32_16x16x32_bf16 v[86:89], v[110:113], v[190:193], v[86:89]
	v_mfma_f32_16x16x32_bf16 v[22:25], v[152:155], v[190:193], v[22:25]
	v_mfma_f32_16x16x32_bf16 v[78:81], v[110:113], v[198:201], v[78:81]
	v_mfma_f32_16x16x32_bf16 v[14:17], v[152:155], v[198:201], v[14:17]
	v_mfma_f32_16x16x32_bf16 v[70:73], v[110:113], v[206:209], v[70:73]
	v_mfma_f32_16x16x32_bf16 v[6:9], v[152:155], v[206:209], v[6:9]
	s_setprio 0
	s_setprio 1
	v_mfma_f32_16x16x32_bf16 v[90:93], v[156:159], v[178:181], v[90:93]
	v_mfma_f32_16x16x32_bf16 v[26:29], v[170:173], v[178:181], v[26:29]
	v_mfma_f32_16x16x32_bf16 v[82:85], v[156:159], v[186:189], v[82:85]
	v_mfma_f32_16x16x32_bf16 v[18:21], v[170:173], v[186:189], v[18:21]
	v_mfma_f32_16x16x32_bf16 v[74:77], v[156:159], v[194:197], v[74:77]
	v_mfma_f32_16x16x32_bf16 v[10:13], v[170:173], v[194:197], v[10:13]
	v_mfma_f32_16x16x32_bf16 v[66:69], v[156:159], v[202:205], v[66:69]
	v_mfma_f32_16x16x32_bf16 v[2:5], v[170:173], v[202:205], v[2:5]
	v_mfma_f32_16x16x32_bf16 v[90:93], v[160:163], v[182:185], v[90:93]
	v_mfma_f32_16x16x32_bf16 v[26:29], v[174:177], v[182:185], v[26:29]
	v_mfma_f32_16x16x32_bf16 v[82:85], v[160:163], v[190:193], v[82:85]
	v_mfma_f32_16x16x32_bf16 v[18:21], v[174:177], v[190:193], v[18:21]
	v_mfma_f32_16x16x32_bf16 v[74:77], v[160:163], v[198:201], v[74:77]
	v_mfma_f32_16x16x32_bf16 v[10:13], v[174:177], v[198:201], v[10:13]
	v_mfma_f32_16x16x32_bf16 v[66:69], v[160:163], v[206:209], v[66:69]
	v_mfma_f32_16x16x32_bf16 v[2:5], v[174:177], v[206:209], v[2:5]
	s_setprio 0
	s_barrier
	s_add_i32 s74, 0, 0x18000
	s_add_i32 s75, 0, 0x1c000
	v_add_u32_e32 v152, s74, v220
	v_add_u32_e32 v174, s75, v220
	ds_read_b128 v[106:109], v152
	ds_read_b128 v[110:113], v152 offset:1024
	ds_read_b128 v[114:117], v152 offset:2048
	ds_read_b128 v[152:155], v152 offset:3072
	ds_read_b128 v[156:159], v174
	ds_read_b128 v[160:163], v174 offset:1024
	ds_read_b128 v[170:173], v174 offset:2048
	ds_read_b128 v[174:177], v174 offset:3072
	s_add_u32 s70, s70, 0x40000
	s_addc_u32 s71, s71, 0
	s_mov_b32 m0, s16
	v_lshl_add_u64 v[216:217], s[70:71], 0, v[144:145]
	ds_read_b128 v[178:181], v222 offset:32768
	ds_read_b128 v[182:185], v222 offset:33792
	ds_read_b128 v[186:189], v222 offset:34816
	ds_read_b128 v[190:193], v222 offset:35840
	ds_read_b128 v[194:197], v222 offset:36864
	ds_read_b128 v[198:201], v222 offset:37888
	ds_read_b128 v[202:205], v222 offset:38912
	ds_read_b128 v[206:209], v222 offset:39936
	global_load_lds_dwordx4 v[216:217], off
	v_lshl_add_u64 v[216:217], s[70:71], 0, v[146:147]
	s_mov_b32 m0, s20
	s_nop 0
	global_load_lds_dwordx4 v[216:217], off
	s_waitcnt vmcnt(8)
	s_waitcnt lgkmcnt(0)
	s_barrier
	s_setprio 1
	s_waitcnt lgkmcnt(0)
	v_mfma_f32_16x16x32_bf16 v[138:141], v[106:109], v[178:181], v[138:141]
	v_mfma_f32_16x16x32_bf16 v[62:65], v[114:117], v[178:181], v[62:65]
	v_mfma_f32_16x16x32_bf16 v[130:133], v[106:109], v[186:189], v[130:133]
	v_mfma_f32_16x16x32_bf16 v[54:57], v[114:117], v[186:189], v[54:57]
	v_mfma_f32_16x16x32_bf16 v[122:125], v[106:109], v[194:197], v[122:125]
	v_mfma_f32_16x16x32_bf16 v[46:49], v[114:117], v[194:197], v[46:49]
	v_mfma_f32_16x16x32_bf16 v[102:105], v[106:109], v[202:205], v[102:105]
	v_mfma_f32_16x16x32_bf16 v[38:41], v[114:117], v[202:205], v[38:41]
	v_mfma_f32_16x16x32_bf16 v[138:141], v[110:113], v[182:185], v[138:141]
	v_mfma_f32_16x16x32_bf16 v[62:65], v[152:155], v[182:185], v[62:65]
	v_mfma_f32_16x16x32_bf16 v[130:133], v[110:113], v[190:193], v[130:133]
	v_mfma_f32_16x16x32_bf16 v[54:57], v[152:155], v[190:193], v[54:57]
	v_mfma_f32_16x16x32_bf16 v[122:125], v[110:113], v[198:201], v[122:125]
	v_mfma_f32_16x16x32_bf16 v[46:49], v[152:155], v[198:201], v[46:49]
	v_mfma_f32_16x16x32_bf16 v[102:105], v[110:113], v[206:209], v[102:105]
	v_mfma_f32_16x16x32_bf16 v[38:41], v[152:155], v[206:209], v[38:41]
	s_setprio 0
	s_setprio 1
	v_mfma_f32_16x16x32_bf16 v[134:137], v[156:159], v[178:181], v[134:137]
	v_mfma_f32_16x16x32_bf16 v[58:61], v[170:173], v[178:181], v[58:61]
	v_mfma_f32_16x16x32_bf16 v[126:129], v[156:159], v[186:189], v[126:129]
	v_mfma_f32_16x16x32_bf16 v[50:53], v[170:173], v[186:189], v[50:53]
	v_mfma_f32_16x16x32_bf16 v[118:121], v[156:159], v[194:197], v[118:121]
	v_mfma_f32_16x16x32_bf16 v[42:45], v[170:173], v[194:197], v[42:45]
	v_mfma_f32_16x16x32_bf16 v[98:101], v[156:159], v[202:205], v[98:101]
	v_mfma_f32_16x16x32_bf16 v[34:37], v[170:173], v[202:205], v[34:37]
	v_mfma_f32_16x16x32_bf16 v[134:137], v[160:163], v[182:185], v[134:137]
	v_mfma_f32_16x16x32_bf16 v[58:61], v[174:177], v[182:185], v[58:61]
	v_mfma_f32_16x16x32_bf16 v[126:129], v[160:163], v[190:193], v[126:129]
	v_mfma_f32_16x16x32_bf16 v[50:53], v[174:177], v[190:193], v[50:53]
	v_mfma_f32_16x16x32_bf16 v[118:121], v[160:163], v[198:201], v[118:121]
	v_mfma_f32_16x16x32_bf16 v[42:45], v[174:177], v[198:201], v[42:45]
	v_mfma_f32_16x16x32_bf16 v[98:101], v[160:163], v[206:209], v[98:101]
	v_mfma_f32_16x16x32_bf16 v[34:37], v[174:177], v[206:209], v[34:37]
	s_setprio 0
	s_barrier
	s_add_i32 s70, s74, s13
	v_lshl_add_u64 v[164:165], v[164:165], 0, s[56:57]
	s_mov_b32 m0, s70
	ds_read_b128 v[178:181], v222 offset:49152
	ds_read_b128 v[182:185], v222 offset:50176
	ds_read_b128 v[186:189], v222 offset:51200
	ds_read_b128 v[190:193], v222 offset:52224
	ds_read_b128 v[194:197], v222 offset:53248
	ds_read_b128 v[198:201], v222 offset:54272
	ds_read_b128 v[202:205], v222 offset:55296
	ds_read_b128 v[206:209], v222 offset:56320
	global_load_lds_dwordx4 v[164:165], off
	s_add_i32 m0, s70, 0x2000
	s_add_u32 s68, s68, 0x8080
	v_lshl_add_u64 v[164:165], v[210:211], 0, s[56:57]
	s_addc_u32 s69, s69, 0
	s_add_i32 s70, s75, s13
	global_load_lds_dwordx4 v[164:165], off
	v_lshl_add_u64 v[164:165], s[68:69], 0, v[166:167]
	s_mov_b32 m0, s70
	s_nop 0
	global_load_lds_dwordx4 v[164:165], off
	v_lshl_add_u64 v[164:165], s[68:69], 0, v[142:143]
	s_add_i32 m0, s70, 0x2000
	s_nop 0
	global_load_lds_dwordx4 v[164:165], off
	v_lshl_add_u64 v[164:165], v[212:213], 0, s[56:57]
	s_mov_b32 m0, s21
	s_nop 0
	global_load_lds_dwordx4 v[164:165], off
	v_lshl_add_u64 v[164:165], v[214:215], 0, s[56:57]
	s_mov_b32 m0, s22
	s_nop 0
	global_load_lds_dwordx4 v[164:165], off
	s_waitcnt vmcnt(8)
	s_waitcnt lgkmcnt(0)
	s_barrier
	s_setprio 1
	s_waitcnt lgkmcnt(0)
	v_mfma_f32_16x16x32_bf16 v[94:97], v[106:109], v[178:181], v[94:97]
	v_mfma_f32_16x16x32_bf16 v[30:33], v[114:117], v[178:181], v[30:33]
	v_mfma_f32_16x16x32_bf16 v[86:89], v[106:109], v[186:189], v[86:89]
	v_mfma_f32_16x16x32_bf16 v[22:25], v[114:117], v[186:189], v[22:25]
	v_mfma_f32_16x16x32_bf16 v[78:81], v[106:109], v[194:197], v[78:81]
	v_mfma_f32_16x16x32_bf16 v[14:17], v[114:117], v[194:197], v[14:17]
	v_mfma_f32_16x16x32_bf16 v[70:73], v[106:109], v[202:205], v[70:73]
	v_mfma_f32_16x16x32_bf16 v[6:9], v[114:117], v[202:205], v[6:9]
	v_mfma_f32_16x16x32_bf16 v[94:97], v[110:113], v[182:185], v[94:97]
	v_mfma_f32_16x16x32_bf16 v[30:33], v[152:155], v[182:185], v[30:33]
	v_mfma_f32_16x16x32_bf16 v[86:89], v[110:113], v[190:193], v[86:89]
	v_mfma_f32_16x16x32_bf16 v[22:25], v[152:155], v[190:193], v[22:25]
	v_mfma_f32_16x16x32_bf16 v[78:81], v[110:113], v[198:201], v[78:81]
	v_mfma_f32_16x16x32_bf16 v[14:17], v[152:155], v[198:201], v[14:17]
	v_mfma_f32_16x16x32_bf16 v[70:73], v[110:113], v[206:209], v[70:73]
	v_mfma_f32_16x16x32_bf16 v[6:9], v[152:155], v[206:209], v[6:9]
	s_setprio 0
	s_setprio 1
	v_mfma_f32_16x16x32_bf16 v[90:93], v[156:159], v[178:181], v[90:93]
	v_mfma_f32_16x16x32_bf16 v[26:29], v[170:173], v[178:181], v[26:29]
	v_mfma_f32_16x16x32_bf16 v[82:85], v[156:159], v[186:189], v[82:85]
	v_mfma_f32_16x16x32_bf16 v[18:21], v[170:173], v[186:189], v[18:21]
	v_mfma_f32_16x16x32_bf16 v[74:77], v[156:159], v[194:197], v[74:77]
	v_mfma_f32_16x16x32_bf16 v[10:13], v[170:173], v[194:197], v[10:13]
	v_mfma_f32_16x16x32_bf16 v[66:69], v[156:159], v[202:205], v[66:69]
	v_mfma_f32_16x16x32_bf16 v[2:5], v[170:173], v[202:205], v[2:5]
	v_mfma_f32_16x16x32_bf16 v[90:93], v[160:163], v[182:185], v[90:93]
	v_mfma_f32_16x16x32_bf16 v[26:29], v[174:177], v[182:185], v[26:29]
	v_mfma_f32_16x16x32_bf16 v[82:85], v[160:163], v[190:193], v[82:85]
	v_mfma_f32_16x16x32_bf16 v[18:21], v[174:177], v[190:193], v[18:21]
	v_mfma_f32_16x16x32_bf16 v[74:77], v[160:163], v[198:201], v[74:77]
	v_mfma_f32_16x16x32_bf16 v[10:13], v[174:177], v[198:201], v[10:13]
	v_mfma_f32_16x16x32_bf16 v[66:69], v[160:163], v[206:209], v[66:69]
	v_mfma_f32_16x16x32_bf16 v[2:5], v[174:177], v[206:209], v[2:5]
	s_setprio 0
	s_barrier
	s_add_u32 s66, s66, 0x100
	s_addc_u32 s72, s72, 0
	s_add_u32 s64, s64, 0x100
	s_addc_u32 s65, s65, 0
	s_cmp_ge_i32 s73, s1
	s_mov_b32 s68, s73
	s_cbranch_scc0 .LBB0_469
.Lpeelexitph3:
	s_branch .LBB0_471
.LBB0_470:
	v_mov_b64_e32 v[4:5], 0
	v_mov_b64_e32 v[2:3], 0
	v_mov_b64_e32 v[68:69], 0
	v_mov_b64_e32 v[66:67], 0
	v_mov_b64_e32 v[12:13], 0
	v_mov_b64_e32 v[10:11], 0
	v_mov_b64_e32 v[76:77], 0
	v_mov_b64_e32 v[74:75], 0
	v_mov_b64_e32 v[140:141], 0
	v_mov_b64_e32 v[138:139], 0
	v_mov_b64_e32 v[64:65], 0
	v_mov_b64_e32 v[62:63], 0
	v_mov_b64_e32 v[132:133], 0
	v_mov_b64_e32 v[130:131], 0
	v_mov_b64_e32 v[56:57], 0
	v_mov_b64_e32 v[54:55], 0
	v_mov_b64_e32 v[124:125], 0
	v_mov_b64_e32 v[122:123], 0
	v_mov_b64_e32 v[48:49], 0
	v_mov_b64_e32 v[46:47], 0
	v_mov_b64_e32 v[104:105], 0
	v_mov_b64_e32 v[102:103], 0
	v_mov_b64_e32 v[40:41], 0
	v_mov_b64_e32 v[38:39], 0
	v_mov_b64_e32 v[136:137], 0
	v_mov_b64_e32 v[134:135], 0
	v_mov_b64_e32 v[60:61], 0
	v_mov_b64_e32 v[58:59], 0
	v_mov_b64_e32 v[128:129], 0
	v_mov_b64_e32 v[126:127], 0
	v_mov_b64_e32 v[52:53], 0
	v_mov_b64_e32 v[50:51], 0
	v_mov_b64_e32 v[120:121], 0
	v_mov_b64_e32 v[118:119], 0
	v_mov_b64_e32 v[44:45], 0
	v_mov_b64_e32 v[42:43], 0
	v_mov_b64_e32 v[100:101], 0
	v_mov_b64_e32 v[98:99], 0
	v_mov_b64_e32 v[36:37], 0
	v_mov_b64_e32 v[34:35], 0
	v_mov_b64_e32 v[96:97], 0
	v_mov_b64_e32 v[94:95], 0
	v_mov_b64_e32 v[32:33], 0
	v_mov_b64_e32 v[30:31], 0
	v_mov_b64_e32 v[88:89], 0
	v_mov_b64_e32 v[86:87], 0
	v_mov_b64_e32 v[24:25], 0
	v_mov_b64_e32 v[22:23], 0
	v_mov_b64_e32 v[80:81], 0
	v_mov_b64_e32 v[78:79], 0
	v_mov_b64_e32 v[16:17], 0
	v_mov_b64_e32 v[14:15], 0
	v_mov_b64_e32 v[72:73], 0
	v_mov_b64_e32 v[70:71], 0
	v_mov_b64_e32 v[8:9], 0
	v_mov_b64_e32 v[6:7], 0
	v_mov_b64_e32 v[92:93], 0
	v_mov_b64_e32 v[90:91], 0
	v_mov_b64_e32 v[28:29], 0
	v_mov_b64_e32 v[26:27], 0
	v_mov_b64_e32 v[84:85], 0
	v_mov_b64_e32 v[82:83], 0
	v_mov_b64_e32 v[20:21], 0
	v_mov_b64_e32 v[18:19], 0

.LBB0_662:
	s_ashr_i32 s59, s58, 31
	s_lshl_b64 s[62:63], s[58:59], 19
	s_add_u32 s62, s10, s62
	s_addc_u32 s63, s11, s63
	s_ashr_i32 s55, s54, 31
	s_lshl_b64 s[64:65], s[54:55], 19
	s_add_u32 s64, s12, s64
	s_addc_u32 s65, s13, s65
	s_andn2_b64 vcc, exec, s[46:47]
	s_cbranch_vccnz .LBB0_752
	s_and_b64 s[74:75], s[60:61], exec
	s_cselect_b32 s29, s63, s69
	s_cselect_b32 s43, s62, s68
	s_cselect_b32 s55, s65, s71
	s_cselect_b32 s59, s64, s70
	s_add_u32 s77, s70, 0x100
	s_addc_u32 s79, s71, 0
	s_add_u32 s74, s68, 0x40080
	s_addc_u32 s75, s69, 0
	s_mov_b32 s68, 0
	s_waitcnt lgkmcnt(0)
.Lpeelph6_0:
	s_add_i32 s84, s68, 2
	s_add_u32 s69, s74, 0xfffc0080
	s_addc_u32 s70, s75, -1
	s_add_i32 s88, 0, 0x10000
	s_cmp_eq_u32 s72, s68
	s_cselect_b32 s71, s29, s70
	s_cselect_b32 s70, s43, s69
	s_cselect_b32 s69, s55, s79
	s_cselect_b32 s68, s59, s77
	s_add_i32 s92, 0, 0x14000
	v_add_u32_e32 v78, s88, v204
	v_add_u32_e32 v170, s92, v204
	ds_read_b128 v[58:61], v78
	ds_read_b128 v[62:65], v78 offset:1024
	ds_read_b128 v[74:77], v78 offset:2048
	ds_read_b128 v[78:81], v78 offset:3072
	ds_read_b128 v[146:149], v170
	ds_read_b128 v[150:153], v170 offset:1024
	ds_read_b128 v[154:157], v170 offset:2048
	ds_read_b128 v[170:173], v170 offset:3072
	v_lshl_add_u64 v[202:203], s[74:75], 0, v[180:181]
	s_add_i32 m0, s15, 0xc000
	ds_read_b128 v[174:177], v208
	ds_read_b128 v[182:185], v208 offset:1024
	ds_read_b128 v[186:189], v208 offset:2048
	ds_read_b128 v[190:193], v208 offset:3072
	ds_read_b128 v[194:197], v208 offset:4096
	ds_read_b128 v[198:201], v208 offset:5120
	ds_read_b128 v[210:213], v208 offset:6144
	ds_read_b128 v[214:217], v208 offset:7168
	global_load_lds_dwordx4 v[202:203], off
	v_lshl_add_u64 v[202:203], s[74:75], 0, v[178:179]
	s_add_i32 m0, s15, 0xe000
	s_nop 0
	global_load_lds_dwordx4 v[202:203], off
	s_waitcnt vmcnt(8)
	s_waitcnt lgkmcnt(0)
	s_barrier
	s_setprio 1
	s_waitcnt lgkmcnt(0)
	v_mfma_f32_16x16x32_bf16 v[142:145], v[58:61], v[174:177], 0
	v_mfma_f32_16x16x32_bf16 v[138:141], v[74:77], v[174:177], 0
	v_mfma_f32_16x16x32_bf16 v[126:129], v[58:61], v[186:189], 0
	v_mfma_f32_16x16x32_bf16 v[122:125], v[74:77], v[186:189], 0
	v_mfma_f32_16x16x32_bf16 v[110:113], v[58:61], v[194:197], 0
	v_mfma_f32_16x16x32_bf16 v[106:109], v[74:77], v[194:197], 0
	v_mfma_f32_16x16x32_bf16 v[94:97], v[58:61], v[210:213], 0
	v_mfma_f32_16x16x32_bf16 v[90:93], v[74:77], v[210:213], 0
	v_mfma_f32_16x16x32_bf16 v[142:145], v[62:65], v[182:185], v[142:145]
	v_mfma_f32_16x16x32_bf16 v[138:141], v[78:81], v[182:185], v[138:141]
	v_mfma_f32_16x16x32_bf16 v[126:129], v[62:65], v[190:193], v[126:129]
	v_mfma_f32_16x16x32_bf16 v[122:125], v[78:81], v[190:193], v[122:125]
	v_mfma_f32_16x16x32_bf16 v[110:113], v[62:65], v[198:201], v[110:113]
	v_mfma_f32_16x16x32_bf16 v[106:109], v[78:81], v[198:201], v[106:109]
	v_mfma_f32_16x16x32_bf16 v[94:97], v[62:65], v[214:217], v[94:97]
	v_mfma_f32_16x16x32_bf16 v[90:93], v[78:81], v[214:217], v[90:93]
	s_setprio 0
	s_setprio 1
	v_mfma_f32_16x16x32_bf16 v[134:137], v[146:149], v[174:177], 0
	v_mfma_f32_16x16x32_bf16 v[130:133], v[154:157], v[174:177], 0
	v_mfma_f32_16x16x32_bf16 v[118:121], v[146:149], v[186:189], 0
	v_mfma_f32_16x16x32_bf16 v[114:117], v[154:157], v[186:189], 0
	v_mfma_f32_16x16x32_bf16 v[102:105], v[146:149], v[194:197], 0
	v_mfma_f32_16x16x32_bf16 v[98:101], v[154:157], v[194:197], 0
	v_mfma_f32_16x16x32_bf16 v[86:89], v[146:149], v[210:213], 0
	v_mfma_f32_16x16x32_bf16 v[82:85], v[154:157], v[210:213], 0
	v_mfma_f32_16x16x32_bf16 v[134:137], v[150:153], v[182:185], v[134:137]
	v_mfma_f32_16x16x32_bf16 v[130:133], v[170:173], v[182:185], v[130:133]
	v_mfma_f32_16x16x32_bf16 v[118:121], v[150:153], v[190:193], v[118:121]
	v_mfma_f32_16x16x32_bf16 v[114:117], v[170:173], v[190:193], v[114:117]
	v_mfma_f32_16x16x32_bf16 v[102:105], v[150:153], v[198:201], v[102:105]
	v_mfma_f32_16x16x32_bf16 v[98:101], v[170:173], v[198:201], v[98:101]
	v_mfma_f32_16x16x32_bf16 v[86:89], v[150:153], v[214:217], v[86:89]
	v_mfma_f32_16x16x32_bf16 v[82:85], v[170:173], v[214:217], v[82:85]
	s_setprio 0
	s_barrier
	s_add_i32 s88, s88, s14
	v_lshl_add_u64 v[202:203], s[68:69], 0, v[166:167]
	s_mov_b32 m0, s88
	ds_read_b128 v[174:177], v208 offset:16384
	ds_read_b128 v[182:185], v208 offset:17408
	ds_read_b128 v[186:189], v208 offset:18432
	ds_read_b128 v[190:193], v208 offset:19456
	ds_read_b128 v[194:197], v208 offset:20480
	ds_read_b128 v[198:201], v208 offset:21504
	ds_read_b128 v[210:213], v208 offset:22528
	ds_read_b128 v[214:217], v208 offset:23552
	global_load_lds_dwordx4 v[202:203], off
	s_add_i32 m0, s88, 0x2000
	s_add_u32 s90, s68, 0x40000
	v_lshl_add_u64 v[218:219], s[68:69], 0, v[158:159]
	s_addc_u32 s91, s69, 0
	s_add_i32 s88, s92, s14
	global_load_lds_dwordx4 v[218:219], off
	v_lshl_add_u64 v[220:221], s[90:91], 0, v[166:167]
	s_mov_b32 m0, s88
	v_lshl_add_u64 v[222:223], s[70:71], 0, v[162:163]
	global_load_lds_dwordx4 v[220:221], off
	v_lshl_add_u64 v[220:221], s[90:91], 0, v[158:159]
	s_add_i32 m0, s88, 0x2000
	s_nop 0
	global_load_lds_dwordx4 v[220:221], off
	v_lshl_add_u64 v[220:221], s[70:71], 0, v[160:161]
	s_mov_b32 m0, s15
	s_nop 0
	global_load_lds_dwordx4 v[220:221], off
	s_mov_b32 m0, s16
	s_nop 0
	global_load_lds_dwordx4 v[222:223], off
	s_waitcnt vmcnt(8)
	s_waitcnt lgkmcnt(0)
	s_barrier
	s_setprio 1
	s_waitcnt lgkmcnt(0)
	v_mfma_f32_16x16x32_bf16 v[70:73], v[58:61], v[174:177], 0
	v_mfma_f32_16x16x32_bf16 v[66:69], v[74:77], v[174:177], 0
	v_mfma_f32_16x16x32_bf16 v[46:49], v[58:61], v[186:189], 0
	v_mfma_f32_16x16x32_bf16 v[42:45], v[74:77], v[186:189], 0
	v_mfma_f32_16x16x32_bf16 v[30:33], v[58:61], v[194:197], 0
	v_mfma_f32_16x16x32_bf16 v[26:29], v[74:77], v[194:197], 0
	v_mfma_f32_16x16x32_bf16 v[14:17], v[58:61], v[210:213], 0
	v_mfma_f32_16x16x32_bf16 v[10:13], v[74:77], v[210:213], 0
	v_mfma_f32_16x16x32_bf16 v[70:73], v[62:65], v[182:185], v[70:73]
	v_mfma_f32_16x16x32_bf16 v[66:69], v[78:81], v[182:185], v[66:69]
	v_mfma_f32_16x16x32_bf16 v[46:49], v[62:65], v[190:193], v[46:49]
	v_mfma_f32_16x16x32_bf16 v[42:45], v[78:81], v[190:193], v[42:45]
	v_mfma_f32_16x16x32_bf16 v[30:33], v[62:65], v[198:201], v[30:33]
	v_mfma_f32_16x16x32_bf16 v[26:29], v[78:81], v[198:201], v[26:29]
	v_mfma_f32_16x16x32_bf16 v[14:17], v[62:65], v[214:217], v[14:17]
	v_mfma_f32_16x16x32_bf16 v[10:13], v[78:81], v[214:217], v[10:13]
	s_setprio 0
	s_setprio 1
	v_mfma_f32_16x16x32_bf16 v[54:57], v[146:149], v[174:177], 0
	v_mfma_f32_16x16x32_bf16 v[50:53], v[154:157], v[174:177], 0
	v_mfma_f32_16x16x32_bf16 v[38:41], v[146:149], v[186:189], 0
	v_mfma_f32_16x16x32_bf16 v[34:37], v[154:157], v[186:189], 0
	v_mfma_f32_16x16x32_bf16 v[22:25], v[146:149], v[194:197], 0
	v_mfma_f32_16x16x32_bf16 v[18:21], v[154:157], v[194:197], 0
	v_mfma_f32_16x16x32_bf16 v[6:9], v[146:149], v[210:213], 0
	v_mfma_f32_16x16x32_bf16 v[2:5], v[154:157], v[210:213], 0
	v_mfma_f32_16x16x32_bf16 v[54:57], v[150:153], v[182:185], v[54:57]
	v_mfma_f32_16x16x32_bf16 v[50:53], v[170:173], v[182:185], v[50:53]
	v_mfma_f32_16x16x32_bf16 v[38:41], v[150:153], v[190:193], v[38:41]
	v_mfma_f32_16x16x32_bf16 v[34:37], v[170:173], v[190:193], v[34:37]
	v_mfma_f32_16x16x32_bf16 v[22:25], v[150:153], v[198:201], v[22:25]
	v_mfma_f32_16x16x32_bf16 v[18:21], v[170:173], v[198:201], v[18:21]
	v_mfma_f32_16x16x32_bf16 v[6:9], v[150:153], v[214:217], v[6:9]
	v_mfma_f32_16x16x32_bf16 v[2:5], v[170:173], v[214:217], v[2:5]
	s_setprio 0
	s_barrier
	s_add_i32 s88, 0, 0x18000
	s_add_i32 s90, 0, 0x1c000
	v_add_u32_e32 v78, s88, v204
	v_add_u32_e32 v170, s90, v204
	ds_read_b128 v[58:61], v78
	ds_read_b128 v[62:65], v78 offset:1024
	ds_read_b128 v[74:77], v78 offset:2048
	ds_read_b128 v[78:81], v78 offset:3072
	ds_read_b128 v[146:149], v170
	ds_read_b128 v[150:153], v170 offset:1024
	ds_read_b128 v[154:157], v170 offset:2048
	ds_read_b128 v[170:173], v170 offset:3072
	s_add_u32 s70, s70, 0x40000
	s_addc_u32 s71, s71, 0
	s_mov_b32 m0, s20
	v_lshl_add_u64 v[232:233], s[70:71], 0, v[160:161]
	ds_read_b128 v[174:177], v208 offset:32768
	ds_read_b128 v[182:185], v208 offset:33792
	ds_read_b128 v[186:189], v208 offset:34816
	ds_read_b128 v[190:193], v208 offset:35840
	ds_read_b128 v[194:197], v208 offset:36864
	ds_read_b128 v[198:201], v208 offset:37888
	ds_read_b128 v[210:213], v208 offset:38912
	ds_read_b128 v[214:217], v208 offset:39936
	global_load_lds_dwordx4 v[232:233], off
	v_lshl_add_u64 v[232:233], s[70:71], 0, v[162:163]
	s_mov_b32 m0, s21
	s_nop 0
	global_load_lds_dwordx4 v[232:233], off
	s_waitcnt vmcnt(8)
	s_waitcnt lgkmcnt(0)
	s_barrier
	s_setprio 1
	s_waitcnt lgkmcnt(0)
	v_mfma_f32_16x16x32_bf16 v[142:145], v[58:61], v[174:177], v[142:145]
	v_mfma_f32_16x16x32_bf16 v[138:141], v[74:77], v[174:177], v[138:141]
	v_mfma_f32_16x16x32_bf16 v[126:129], v[58:61], v[186:189], v[126:129]
	v_mfma_f32_16x16x32_bf16 v[122:125], v[74:77], v[186:189], v[122:125]
	v_mfma_f32_16x16x32_bf16 v[110:113], v[58:61], v[194:197], v[110:113]
	v_mfma_f32_16x16x32_bf16 v[106:109], v[74:77], v[194:197], v[106:109]
	v_mfma_f32_16x16x32_bf16 v[94:97], v[58:61], v[210:213], v[94:97]
	v_mfma_f32_16x16x32_bf16 v[90:93], v[74:77], v[210:213], v[90:93]
	v_mfma_f32_16x16x32_bf16 v[142:145], v[62:65], v[182:185], v[142:145]
	v_mfma_f32_16x16x32_bf16 v[138:141], v[78:81], v[182:185], v[138:141]
	v_mfma_f32_16x16x32_bf16 v[126:129], v[62:65], v[190:193], v[126:129]
	v_mfma_f32_16x16x32_bf16 v[122:125], v[78:81], v[190:193], v[122:125]
	v_mfma_f32_16x16x32_bf16 v[110:113], v[62:65], v[198:201], v[110:113]
	v_mfma_f32_16x16x32_bf16 v[106:109], v[78:81], v[198:201], v[106:109]
	v_mfma_f32_16x16x32_bf16 v[94:97], v[62:65], v[214:217], v[94:97]
	v_mfma_f32_16x16x32_bf16 v[90:93], v[78:81], v[214:217], v[90:93]
	s_setprio 0
	s_setprio 1
	v_mfma_f32_16x16x32_bf16 v[134:137], v[146:149], v[174:177], v[134:137]
	v_mfma_f32_16x16x32_bf16 v[130:133], v[154:157], v[174:177], v[130:133]
	v_mfma_f32_16x16x32_bf16 v[118:121], v[146:149], v[186:189], v[118:121]
	v_mfma_f32_16x16x32_bf16 v[114:117], v[154:157], v[186:189], v[114:117]
	v_mfma_f32_16x16x32_bf16 v[102:105], v[146:149], v[194:197], v[102:105]
	v_mfma_f32_16x16x32_bf16 v[98:101], v[154:157], v[194:197], v[98:101]
	v_mfma_f32_16x16x32_bf16 v[86:89], v[146:149], v[210:213], v[86:89]
	v_mfma_f32_16x16x32_bf16 v[82:85], v[154:157], v[210:213], v[82:85]
	v_mfma_f32_16x16x32_bf16 v[134:137], v[150:153], v[182:185], v[134:137]
	v_mfma_f32_16x16x32_bf16 v[130:133], v[170:173], v[182:185], v[130:133]
	v_mfma_f32_16x16x32_bf16 v[118:121], v[150:153], v[190:193], v[118:121]
	v_mfma_f32_16x16x32_bf16 v[114:117], v[170:173], v[190:193], v[114:117]
	v_mfma_f32_16x16x32_bf16 v[102:105], v[150:153], v[198:201], v[102:105]
	v_mfma_f32_16x16x32_bf16 v[98:101], v[170:173], v[198:201], v[98:101]
	v_mfma_f32_16x16x32_bf16 v[86:89], v[150:153], v[214:217], v[86:89]
	v_mfma_f32_16x16x32_bf16 v[82:85], v[170:173], v[214:217], v[82:85]
	s_setprio 0
	s_barrier
	s_add_i32 s70, s88, s14
	v_lshl_add_u64 v[202:203], v[202:203], 0, s[56:57]
	s_mov_b32 m0, s70
	ds_read_b128 v[174:177], v208 offset:49152
	ds_read_b128 v[182:185], v208 offset:50176
	ds_read_b128 v[186:189], v208 offset:51200
	ds_read_b128 v[190:193], v208 offset:52224
	ds_read_b128 v[194:197], v208 offset:53248
	ds_read_b128 v[198:201], v208 offset:54272
	ds_read_b128 v[210:213], v208 offset:55296
	ds_read_b128 v[214:217], v208 offset:56320
	global_load_lds_dwordx4 v[202:203], off
	s_add_i32 m0, s70, 0x2000
	s_add_u32 s68, s68, 0x40080
	v_lshl_add_u64 v[202:203], v[218:219], 0, s[56:57]
	s_addc_u32 s69, s69, 0
	s_add_i32 s70, s90, s14
	global_load_lds_dwordx4 v[202:203], off
	v_lshl_add_u64 v[202:203], s[68:69], 0, v[166:167]
	s_mov_b32 m0, s70
	s_nop 0
	global_load_lds_dwordx4 v[202:203], off
	v_lshl_add_u64 v[202:203], s[68:69], 0, v[158:159]
	s_add_i32 m0, s70, 0x2000
	s_nop 0
	global_load_lds_dwordx4 v[202:203], off
	v_lshl_add_u64 v[202:203], v[220:221], 0, s[56:57]
	s_mov_b32 m0, s24
	s_nop 0
	global_load_lds_dwordx4 v[202:203], off
	v_lshl_add_u64 v[202:203], v[222:223], 0, s[56:57]
	s_mov_b32 m0, s25
	s_nop 0
	global_load_lds_dwordx4 v[202:203], off
	s_waitcnt vmcnt(8)
	s_waitcnt lgkmcnt(0)
	s_barrier
	s_setprio 1
	s_waitcnt lgkmcnt(0)
	v_mfma_f32_16x16x32_bf16 v[70:73], v[58:61], v[174:177], v[70:73]
	v_mfma_f32_16x16x32_bf16 v[66:69], v[74:77], v[174:177], v[66:69]
	v_mfma_f32_16x16x32_bf16 v[46:49], v[58:61], v[186:189], v[46:49]
	v_mfma_f32_16x16x32_bf16 v[42:45], v[74:77], v[186:189], v[42:45]
	v_mfma_f32_16x16x32_bf16 v[30:33], v[58:61], v[194:197], v[30:33]
	v_mfma_f32_16x16x32_bf16 v[26:29], v[74:77], v[194:197], v[26:29]
	v_mfma_f32_16x16x32_bf16 v[14:17], v[58:61], v[210:213], v[14:17]
	v_mfma_f32_16x16x32_bf16 v[10:13], v[74:77], v[210:213], v[10:13]
	v_mfma_f32_16x16x32_bf16 v[70:73], v[62:65], v[182:185], v[70:73]
	v_mfma_f32_16x16x32_bf16 v[66:69], v[78:81], v[182:185], v[66:69]
	v_mfma_f32_16x16x32_bf16 v[46:49], v[62:65], v[190:193], v[46:49]
	v_mfma_f32_16x16x32_bf16 v[42:45], v[78:81], v[190:193], v[42:45]
	v_mfma_f32_16x16x32_bf16 v[30:33], v[62:65], v[198:201], v[30:33]
	v_mfma_f32_16x16x32_bf16 v[26:29], v[78:81], v[198:201], v[26:29]
	v_mfma_f32_16x16x32_bf16 v[14:17], v[62:65], v[214:217], v[14:17]
	v_mfma_f32_16x16x32_bf16 v[10:13], v[78:81], v[214:217], v[10:13]
	s_setprio 0
	s_setprio 1
	v_mfma_f32_16x16x32_bf16 v[54:57], v[146:149], v[174:177], v[54:57]
	v_mfma_f32_16x16x32_bf16 v[50:53], v[154:157], v[174:177], v[50:53]
	v_mfma_f32_16x16x32_bf16 v[38:41], v[146:149], v[186:189], v[38:41]
	v_mfma_f32_16x16x32_bf16 v[34:37], v[154:157], v[186:189], v[34:37]
	v_mfma_f32_16x16x32_bf16 v[22:25], v[146:149], v[194:197], v[22:25]
	v_mfma_f32_16x16x32_bf16 v[18:21], v[154:157], v[194:197], v[18:21]
	v_mfma_f32_16x16x32_bf16 v[6:9], v[146:149], v[210:213], v[6:9]
	v_mfma_f32_16x16x32_bf16 v[2:5], v[154:157], v[210:213], v[2:5]
	v_mfma_f32_16x16x32_bf16 v[54:57], v[150:153], v[182:185], v[54:57]
	v_mfma_f32_16x16x32_bf16 v[50:53], v[170:173], v[182:185], v[50:53]
	v_mfma_f32_16x16x32_bf16 v[38:41], v[150:153], v[190:193], v[38:41]
	v_mfma_f32_16x16x32_bf16 v[34:37], v[170:173], v[190:193], v[34:37]
	v_mfma_f32_16x16x32_bf16 v[22:25], v[150:153], v[198:201], v[22:25]
	v_mfma_f32_16x16x32_bf16 v[18:21], v[170:173], v[198:201], v[18:21]
	v_mfma_f32_16x16x32_bf16 v[6:9], v[150:153], v[214:217], v[6:9]
	v_mfma_f32_16x16x32_bf16 v[2:5], v[170:173], v[214:217], v[2:5]
	s_setprio 0
	s_barrier
	s_add_u32 s77, s77, 0x100
	s_addc_u32 s79, s79, 0
	s_add_u32 s74, s74, 0x100
	s_addc_u32 s75, s75, 0
	s_cmp_ge_i32 s84, s1
	s_mov_b32 s68, s84
	s_cbranch_scc0 .LBB0_664
	s_branch .Lpeelexitph6

.Lpeelexitph6:
	s_movk_i32 s79, 0x1ff
	s_mov_b32 s84, 0xf800000
	s_mov_b32 s88, 0xe800000
	s_and_b64 vcc, exec, s[48:49]
	s_cbranch_vccz .LBB0_667

.LBB0_923:
	s_add_u32 s73, s60, 0x100
	v_mov_b32_e32 v1, 0x3ecc95a3
	s_addc_u32 s74, s61, 0
	s_mov_b32 s62, 0
.Lpeelph8_0:
	s_add_i32 s75, s62, 2
	s_add_u32 s60, s58, 0x100
	s_addc_u32 s61, s59, 0
	s_add_i32 s76, 0, 0x10000
	s_cmp_eq_u32 s68, s62
	s_cselect_b32 s65, s53, s61
	s_cselect_b32 s64, s52, s60
	s_cselect_b32 s63, s55, s74
	s_cselect_b32 s62, s54, s73
	s_add_i32 s77, 0, 0x14000
	v_add_u32_e32 v2, s76, v200
	v_add_u32_e32 v6, s77, v200
	ds_read_b128 v[26:29], v2
	ds_read_b128 v[30:33], v2 offset:1024
	ds_read_b128 v[18:21], v2 offset:2048
	ds_read_b128 v[22:25], v2 offset:3072
	ds_read_b128 v[10:13], v6
	ds_read_b128 v[14:17], v6 offset:1024
	s_waitcnt lgkmcnt(0)
	ds_read_b128 v[2:5], v6 offset:2048
	ds_read_b128 v[6:9], v6 offset:3072
	v_lshl_add_u64 v[170:171], s[58:59], 0, v[184:185]
	s_add_i32 m0, s15, 0xc000
	ds_read_b128 v[186:189], v204
	ds_read_b128 v[190:193], v204 offset:1024
	ds_read_b128 v[206:209], v204 offset:2048
	ds_read_b128 v[210:213], v204 offset:3072
	ds_read_b128 v[214:217], v204 offset:4096
	ds_read_b128 v[218:221], v204 offset:5120
	ds_read_b128 v[236:239], v204 offset:6144
	ds_read_b128 v[240:243], v204 offset:7168
	global_load_lds_dwordx4 v[170:171], off
	v_lshl_add_u64 v[170:171], s[58:59], 0, v[182:183]
	s_add_i32 m0, s15, 0xe000
	s_nop 0
	global_load_lds_dwordx4 v[170:171], off
	s_waitcnt vmcnt(8)
	s_waitcnt lgkmcnt(0)
	s_barrier
	s_setprio 1
	s_waitcnt lgkmcnt(0)
	v_mfma_scale_f32_16x16x128_f8f6f4 v[158:161], v[26:33], v[186:193], 0, v198, v169 op_sel_hi:[0,0,0]
	v_mfma_scale_f32_16x16x128_f8f6f4 v[154:157], v[18:25], v[186:193], 0, v198, v169 op_sel_hi:[0,0,0]
	v_mfma_scale_f32_16x16x128_f8f6f4 v[142:145], v[26:33], v[206:213], 0, v198, v169 op_sel_hi:[0,0,0]
	v_mfma_scale_f32_16x16x128_f8f6f4 v[138:141], v[18:25], v[206:213], 0, v198, v169 op_sel_hi:[0,0,0]
	v_mfma_scale_f32_16x16x128_f8f6f4 v[126:129], v[26:33], v[214:221], 0, v198, v169 op_sel_hi:[0,0,0]
	v_mfma_scale_f32_16x16x128_f8f6f4 v[122:125], v[18:25], v[214:221], 0, v198, v169 op_sel_hi:[0,0,0]
	v_mfma_scale_f32_16x16x128_f8f6f4 v[110:113], v[26:33], v[236:243], 0, v198, v169 op_sel_hi:[0,0,0]
	v_mfma_scale_f32_16x16x128_f8f6f4 v[106:109], v[18:25], v[236:243], 0, v198, v169 op_sel_hi:[0,0,0]
	s_setprio 0
	s_setprio 1
	v_mfma_scale_f32_16x16x128_f8f6f4 v[150:153], v[10:17], v[186:193], 0, v198, v169 op_sel_hi:[0,0,0]
	v_mfma_scale_f32_16x16x128_f8f6f4 v[146:149], v[2:9], v[186:193], 0, v198, v169 op_sel_hi:[0,0,0]
	v_mfma_scale_f32_16x16x128_f8f6f4 v[134:137], v[10:17], v[206:213], 0, v198, v169 op_sel_hi:[0,0,0]
	v_mfma_scale_f32_16x16x128_f8f6f4 v[130:133], v[2:9], v[206:213], 0, v198, v169 op_sel_hi:[0,0,0]
	v_mfma_scale_f32_16x16x128_f8f6f4 v[118:121], v[10:17], v[214:221], 0, v198, v169 op_sel_hi:[0,0,0]
	v_mfma_scale_f32_16x16x128_f8f6f4 v[114:117], v[2:9], v[214:221], 0, v198, v169 op_sel_hi:[0,0,0]
	v_mfma_scale_f32_16x16x128_f8f6f4 v[102:105], v[10:17], v[236:243], 0, v198, v169 op_sel_hi:[0,0,0]
	v_mfma_scale_f32_16x16x128_f8f6f4 v[98:101], v[2:9], v[236:243], 0, v198, v169 op_sel_hi:[0,0,0]
	s_setprio 0
	s_barrier
	s_add_i32 s58, s76, s14
	v_lshl_add_u64 v[186:187], s[62:63], 0, v[166:167]
	s_mov_b32 m0, s58
	ds_read_b128 v[206:209], v204 offset:16384
	ds_read_b128 v[210:213], v204 offset:17408
	ds_read_b128 v[214:217], v204 offset:18432
	ds_read_b128 v[218:221], v204 offset:19456
	ds_read_b128 v[236:239], v204 offset:20480
	ds_read_b128 v[240:243], v204 offset:21504
	ds_read_b128 v[244:247], v204 offset:22528
	ds_read_b128 v[248:251], v204 offset:23552
	global_load_lds_dwordx4 v[186:187], off
	s_add_i32 m0, s58, 0x2000
	s_add_u32 s58, s62, 0x70000
	v_lshl_add_u64 v[188:189], s[62:63], 0, v[162:163]
	s_addc_u32 s59, s63, 0
	s_add_i32 s76, s77, s14
	global_load_lds_dwordx4 v[188:189], off
	v_lshl_add_u64 v[170:171], s[58:59], 0, v[166:167]
	s_mov_b32 m0, s76
	v_lshl_add_u64 v[190:191], s[64:65], 0, v[164:165]
	global_load_lds_dwordx4 v[170:171], off
	v_lshl_add_u64 v[170:171], s[58:59], 0, v[162:163]
	s_add_i32 m0, s76, 0x2000
	v_lshl_add_u64 v[192:193], s[64:65], 0, v[178:179]
	global_load_lds_dwordx4 v[170:171], off
	s_mov_b32 m0, s15
	s_nop 0
	global_load_lds_dwordx4 v[190:191], off
	s_mov_b32 m0, s16
	s_nop 0
	global_load_lds_dwordx4 v[192:193], off
	s_waitcnt vmcnt(8)
	s_waitcnt lgkmcnt(0)
	s_barrier
	s_setprio 1
	s_waitcnt lgkmcnt(0)
	v_mfma_scale_f32_16x16x128_f8f6f4 v[94:97], v[26:33], v[206:213], 0, v198, v169 op_sel_hi:[0,0,0]
	v_mfma_scale_f32_16x16x128_f8f6f4 v[90:93], v[18:25], v[206:213], 0, v198, v169 op_sel_hi:[0,0,0]
	v_mfma_scale_f32_16x16x128_f8f6f4 v[78:81], v[26:33], v[214:221], 0, v198, v169 op_sel_hi:[0,0,0]
	v_mfma_scale_f32_16x16x128_f8f6f4 v[74:77], v[18:25], v[214:221], 0, v198, v169 op_sel_hi:[0,0,0]
	v_mfma_scale_f32_16x16x128_f8f6f4 v[62:65], v[26:33], v[236:243], 0, v198, v169 op_sel_hi:[0,0,0]
	v_mfma_scale_f32_16x16x128_f8f6f4 v[58:61], v[18:25], v[236:243], 0, v198, v169 op_sel_hi:[0,0,0]
	v_mfma_scale_f32_16x16x128_f8f6f4 v[46:49], v[26:33], v[244:251], 0, v198, v169 op_sel_hi:[0,0,0]
	v_mfma_scale_f32_16x16x128_f8f6f4 v[42:45], v[18:25], v[244:251], 0, v198, v169 op_sel_hi:[0,0,0]
	s_setprio 0
	s_setprio 1
	v_mfma_scale_f32_16x16x128_f8f6f4 v[86:89], v[10:17], v[206:213], 0, v198, v169 op_sel_hi:[0,0,0]
	v_mfma_scale_f32_16x16x128_f8f6f4 v[82:85], v[2:9], v[206:213], 0, v198, v169 op_sel_hi:[0,0,0]
	v_mfma_scale_f32_16x16x128_f8f6f4 v[70:73], v[10:17], v[214:221], 0, v198, v169 op_sel_hi:[0,0,0]
	v_mfma_scale_f32_16x16x128_f8f6f4 v[66:69], v[2:9], v[214:221], 0, v198, v169 op_sel_hi:[0,0,0]
	v_mfma_scale_f32_16x16x128_f8f6f4 v[54:57], v[10:17], v[236:243], 0, v198, v169 op_sel_hi:[0,0,0]
	v_mfma_scale_f32_16x16x128_f8f6f4 v[50:53], v[2:9], v[236:243], 0, v198, v169 op_sel_hi:[0,0,0]
	v_mfma_scale_f32_16x16x128_f8f6f4 v[38:41], v[10:17], v[244:251], 0, v198, v169 op_sel_hi:[0,0,0]
	v_mfma_scale_f32_16x16x128_f8f6f4 v[34:37], v[2:9], v[244:251], 0, v198, v169 op_sel_hi:[0,0,0]
	s_setprio 0
	s_barrier
	s_add_i32 s76, 0, 0x18000
	s_add_i32 s77, 0, 0x1c000
	v_add_u32_e32 v2, s76, v200
	v_add_u32_e32 v6, s77, v200
	ds_read_b128 v[26:29], v2
	ds_read_b128 v[30:33], v2 offset:1024
	ds_read_b128 v[18:21], v2 offset:2048
	ds_read_b128 v[22:25], v2 offset:3072
	ds_read_b128 v[10:13], v6
	ds_read_b128 v[14:17], v6 offset:1024
	ds_read_b128 v[2:5], v6 offset:2048
	ds_read_b128 v[6:9], v6 offset:3072
	s_add_u32 s58, s64, 0x70000
	s_addc_u32 s59, s65, 0
	s_mov_b32 m0, s20
	v_lshl_add_u64 v[170:171], s[58:59], 0, v[164:165]
	ds_read_b128 v[206:209], v204 offset:32768
	ds_read_b128 v[210:213], v204 offset:33792
	ds_read_b128 v[214:217], v204 offset:34816
	ds_read_b128 v[218:221], v204 offset:35840
	ds_read_b128 v[236:239], v204 offset:36864
	ds_read_b128 v[240:243], v204 offset:37888
	ds_read_b128 v[244:247], v204 offset:38912
	ds_read_b128 v[248:251], v204 offset:39936
	global_load_lds_dwordx4 v[170:171], off
	v_lshl_add_u64 v[170:171], s[58:59], 0, v[178:179]
	s_mov_b32 m0, s21
	s_nop 0
	global_load_lds_dwordx4 v[170:171], off
	s_waitcnt vmcnt(8)
	s_waitcnt lgkmcnt(0)
	s_barrier
	s_setprio 1
	s_waitcnt lgkmcnt(0)
	v_mfma_scale_f32_16x16x128_f8f6f4 v[158:161], v[26:33], v[206:213], v[158:161], v198, v169 op_sel_hi:[0,0,0]
	v_mfma_scale_f32_16x16x128_f8f6f4 v[154:157], v[18:25], v[206:213], v[154:157], v198, v169 op_sel_hi:[0,0,0]
	v_mfma_scale_f32_16x16x128_f8f6f4 v[142:145], v[26:33], v[214:221], v[142:145], v198, v169 op_sel_hi:[0,0,0]
	v_mfma_scale_f32_16x16x128_f8f6f4 v[138:141], v[18:25], v[214:221], v[138:141], v198, v169 op_sel_hi:[0,0,0]
	v_mfma_scale_f32_16x16x128_f8f6f4 v[126:129], v[26:33], v[236:243], v[126:129], v198, v169 op_sel_hi:[0,0,0]
	v_mfma_scale_f32_16x16x128_f8f6f4 v[122:125], v[18:25], v[236:243], v[122:125], v198, v169 op_sel_hi:[0,0,0]
	v_mfma_scale_f32_16x16x128_f8f6f4 v[110:113], v[26:33], v[244:251], v[110:113], v198, v169 op_sel_hi:[0,0,0]
	v_mfma_scale_f32_16x16x128_f8f6f4 v[106:109], v[18:25], v[244:251], v[106:109], v198, v169 op_sel_hi:[0,0,0]
	s_setprio 0
	s_setprio 1
	v_mfma_scale_f32_16x16x128_f8f6f4 v[150:153], v[10:17], v[206:213], v[150:153], v198, v169 op_sel_hi:[0,0,0]
	v_mfma_scale_f32_16x16x128_f8f6f4 v[146:149], v[2:9], v[206:213], v[146:149], v198, v169 op_sel_hi:[0,0,0]
	v_mfma_scale_f32_16x16x128_f8f6f4 v[134:137], v[10:17], v[214:221], v[134:137], v198, v169 op_sel_hi:[0,0,0]
	v_mfma_scale_f32_16x16x128_f8f6f4 v[130:133], v[2:9], v[214:221], v[130:133], v198, v169 op_sel_hi:[0,0,0]
	v_mfma_scale_f32_16x16x128_f8f6f4 v[118:121], v[10:17], v[236:243], v[118:121], v198, v169 op_sel_hi:[0,0,0]
	v_mfma_scale_f32_16x16x128_f8f6f4 v[114:117], v[2:9], v[236:243], v[114:117], v198, v169 op_sel_hi:[0,0,0]
	v_mfma_scale_f32_16x16x128_f8f6f4 v[102:105], v[10:17], v[244:251], v[102:105], v198, v169 op_sel_hi:[0,0,0]
	v_mfma_scale_f32_16x16x128_f8f6f4 v[98:101], v[2:9], v[244:251], v[98:101], v198, v169 op_sel_hi:[0,0,0]
	s_setprio 0
	s_barrier
	s_add_i32 s58, s76, s14
	v_lshl_add_u64 v[170:171], v[186:187], 0, s[56:57]
	s_mov_b32 m0, s58
	ds_read_b128 v[206:209], v204 offset:49152
	ds_read_b128 v[210:213], v204 offset:50176
	ds_read_b128 v[214:217], v204 offset:51200
	ds_read_b128 v[218:221], v204 offset:52224
	ds_read_b128 v[236:239], v204 offset:53248
	ds_read_b128 v[240:243], v204 offset:54272
	ds_read_b128 v[244:247], v204 offset:55296
	ds_read_b128 v[248:251], v204 offset:56320
	global_load_lds_dwordx4 v[170:171], off
	s_add_i32 m0, s58, 0x2000
	s_add_u32 s58, s62, 0x70080
	v_lshl_add_u64 v[170:171], v[188:189], 0, s[56:57]
	s_addc_u32 s59, s63, 0
	s_add_i32 s62, s77, s14
	global_load_lds_dwordx4 v[170:171], off
	v_lshl_add_u64 v[170:171], s[58:59], 0, v[166:167]
	s_mov_b32 m0, s62
	s_nop 0
	global_load_lds_dwordx4 v[170:171], off
	v_lshl_add_u64 v[170:171], s[58:59], 0, v[162:163]
	s_add_i32 m0, s62, 0x2000
	s_nop 0
	global_load_lds_dwordx4 v[170:171], off
	v_lshl_add_u64 v[170:171], v[190:191], 0, s[56:57]
	s_mov_b32 m0, s24
	s_nop 0
	global_load_lds_dwordx4 v[170:171], off
	v_lshl_add_u64 v[170:171], v[192:193], 0, s[56:57]
	s_mov_b32 m0, s25
	s_nop 0
	global_load_lds_dwordx4 v[170:171], off
	s_waitcnt vmcnt(8)
	s_waitcnt lgkmcnt(0)
	s_barrier
	s_setprio 1
	s_waitcnt lgkmcnt(0)
	v_mfma_scale_f32_16x16x128_f8f6f4 v[94:97], v[26:33], v[206:213], v[94:97], v198, v169 op_sel_hi:[0,0,0]
	v_mfma_scale_f32_16x16x128_f8f6f4 v[90:93], v[18:25], v[206:213], v[90:93], v198, v169 op_sel_hi:[0,0,0]
	v_mfma_scale_f32_16x16x128_f8f6f4 v[78:81], v[26:33], v[214:221], v[78:81], v198, v169 op_sel_hi:[0,0,0]
	v_mfma_scale_f32_16x16x128_f8f6f4 v[74:77], v[18:25], v[214:221], v[74:77], v198, v169 op_sel_hi:[0,0,0]
	v_mfma_scale_f32_16x16x128_f8f6f4 v[62:65], v[26:33], v[236:243], v[62:65], v198, v169 op_sel_hi:[0,0,0]
	v_mfma_scale_f32_16x16x128_f8f6f4 v[58:61], v[18:25], v[236:243], v[58:61], v198, v169 op_sel_hi:[0,0,0]
	v_mfma_scale_f32_16x16x128_f8f6f4 v[46:49], v[26:33], v[244:251], v[46:49], v198, v169 op_sel_hi:[0,0,0]
	v_mfma_scale_f32_16x16x128_f8f6f4 v[42:45], v[18:25], v[244:251], v[42:45], v198, v169 op_sel_hi:[0,0,0]
	s_setprio 0
	s_setprio 1
	v_mfma_scale_f32_16x16x128_f8f6f4 v[86:89], v[10:17], v[206:213], v[86:89], v198, v169 op_sel_hi:[0,0,0]
	v_mfma_scale_f32_16x16x128_f8f6f4 v[82:85], v[2:9], v[206:213], v[82:85], v198, v169 op_sel_hi:[0,0,0]
	v_mfma_scale_f32_16x16x128_f8f6f4 v[70:73], v[10:17], v[214:221], v[70:73], v198, v169 op_sel_hi:[0,0,0]
	v_mfma_scale_f32_16x16x128_f8f6f4 v[66:69], v[2:9], v[214:221], v[66:69], v198, v169 op_sel_hi:[0,0,0]
	v_mfma_scale_f32_16x16x128_f8f6f4 v[54:57], v[10:17], v[236:243], v[54:57], v198, v169 op_sel_hi:[0,0,0]
	v_mfma_scale_f32_16x16x128_f8f6f4 v[50:53], v[2:9], v[236:243], v[50:53], v198, v169 op_sel_hi:[0,0,0]
	v_mfma_scale_f32_16x16x128_f8f6f4 v[38:41], v[10:17], v[244:251], v[38:41], v198, v169 op_sel_hi:[0,0,0]
	v_mfma_scale_f32_16x16x128_f8f6f4 v[34:37], v[2:9], v[244:251], v[34:37], v198, v169 op_sel_hi:[0,0,0]
	s_setprio 0
	s_barrier
	s_add_u32 s73, s73, 0x100
	s_addc_u32 s74, s74, 0
	s_cmp_ge_i32 s75, s1
	s_mov_b64 s[58:59], s[60:61]
	s_mov_b32 s62, s75
	s_cbranch_scc0 .LBB0_924
	s_branch .Lpeelexitph8

.Lpeelexitph8:
	v_mov_b32_e32 v209, v1
	s_and_b64 vcc, exec, s[46:47]
	s_cbranch_vccz .LBB0_927

.LBB0_1436:
	s_ashr_i32 s43, s42, 31
	s_lshl_b64 s[46:47], s[42:43], 19
	s_add_u32 s46, s11, s46
	s_addc_u32 s47, s12, s47
	s_ashr_i32 s41, s40, 31
	s_lshl_b64 s[48:49], s[40:41], 19
	s_add_u32 s48, s13, s48
	s_addc_u32 s49, s14, s49
	s_andn2_b64 vcc, exec, s[30:31]
	s_cbranch_vccnz .LBB0_1444
	s_and_b64 s[58:59], s[44:45], exec
	s_cselect_b32 s41, s47, s53
	s_cselect_b32 s43, s46, s52
	s_cselect_b32 s62, s49, s55
	s_cselect_b32 s63, s48, s54
	s_add_u32 s64, s54, 0x100
	s_addc_u32 s65, s55, 0
	s_add_u32 s52, s52, 0x40080
	v_mov_b32_e32 v1, 0x3ecc95a3
	s_addc_u32 s53, s53, 0
	s_mov_b32 s54, 0
.Lpeelph12_0:
	s_add_i32 s66, s54, 2
	s_add_u32 s55, s52, 0xfffc0080
	s_addc_u32 s58, s53, -1
	s_add_i32 s68, 0, 0x10000
	s_cmp_eq_u32 s60, s54
	s_cselect_b32 s59, s41, s58
	s_cselect_b32 s58, s43, s55
	v_add_u32_e32 v144, s68, v147
	s_cselect_b32 s55, s62, s65
	s_cselect_b32 s54, s63, s64
	s_add_i32 s70, 0, 0x14000
	ds_read_b128 v[140:143], v144
	ds_read_b128 v[150:153], v144 offset:1024
	ds_read_b128 v[154:157], v144 offset:2048
	ds_read_b128 v[158:161], v144 offset:3072
	v_add_u32_e32 v144, s70, v147
	ds_read_b128 v[162:165], v144
	ds_read_b128 v[170:173], v144 offset:1024
	ds_read_b128 v[174:177], v144 offset:2048
	ds_read_b128 v[178:181], v144 offset:3072
	v_lshl_add_u64 v[144:145], s[52:53], 0, v[138:139]
	s_add_i32 m0, s16, 0xc000
	ds_read_b128 v[182:185], v149
	ds_read_b128 v[186:189], v149 offset:1024
	ds_read_b128 v[190:193], v149 offset:2048
	ds_read_b128 v[194:197], v149 offset:3072
	ds_read_b128 v[198:201], v149 offset:4096
	ds_read_b128 v[202:205], v149 offset:5120
	ds_read_b128 v[206:209], v149 offset:6144
	ds_read_b128 v[210:213], v149 offset:7168
	global_load_lds_dwordx4 v[144:145], off
	v_lshl_add_u64 v[144:145], s[52:53], 0, v[136:137]
	s_add_i32 m0, s16, 0xe000
	s_nop 0
	global_load_lds_dwordx4 v[144:145], off
	s_waitcnt vmcnt(8)
	s_waitcnt lgkmcnt(0)
	s_barrier
	s_setprio 1
	s_waitcnt lgkmcnt(0)
	v_mfma_f32_16x16x32_bf16 v[126:129], v[140:143], v[182:185], 0
	v_mfma_f32_16x16x32_bf16 v[122:125], v[154:157], v[182:185], 0
	v_mfma_f32_16x16x32_bf16 v[110:113], v[140:143], v[190:193], 0
	v_mfma_f32_16x16x32_bf16 v[106:109], v[154:157], v[190:193], 0
	v_mfma_f32_16x16x32_bf16 v[94:97], v[140:143], v[198:201], 0
	v_mfma_f32_16x16x32_bf16 v[90:93], v[154:157], v[198:201], 0
	v_mfma_f32_16x16x32_bf16 v[78:81], v[140:143], v[206:209], 0
	v_mfma_f32_16x16x32_bf16 v[74:77], v[154:157], v[206:209], 0
	v_mfma_f32_16x16x32_bf16 v[126:129], v[150:153], v[186:189], v[126:129]
	v_mfma_f32_16x16x32_bf16 v[122:125], v[158:161], v[186:189], v[122:125]
	v_mfma_f32_16x16x32_bf16 v[110:113], v[150:153], v[194:197], v[110:113]
	v_mfma_f32_16x16x32_bf16 v[106:109], v[158:161], v[194:197], v[106:109]
	v_mfma_f32_16x16x32_bf16 v[94:97], v[150:153], v[202:205], v[94:97]
	v_mfma_f32_16x16x32_bf16 v[90:93], v[158:161], v[202:205], v[90:93]
	v_mfma_f32_16x16x32_bf16 v[78:81], v[150:153], v[210:213], v[78:81]
	v_mfma_f32_16x16x32_bf16 v[74:77], v[158:161], v[210:213], v[74:77]
	s_setprio 0
	s_setprio 1
	v_mfma_f32_16x16x32_bf16 v[118:121], v[162:165], v[182:185], 0
	v_mfma_f32_16x16x32_bf16 v[114:117], v[174:177], v[182:185], 0
	v_mfma_f32_16x16x32_bf16 v[102:105], v[162:165], v[190:193], 0
	v_mfma_f32_16x16x32_bf16 v[98:101], v[174:177], v[190:193], 0
	v_mfma_f32_16x16x32_bf16 v[86:89], v[162:165], v[198:201], 0
	v_mfma_f32_16x16x32_bf16 v[82:85], v[174:177], v[198:201], 0
	v_mfma_f32_16x16x32_bf16 v[70:73], v[162:165], v[206:209], 0
	v_mfma_f32_16x16x32_bf16 v[66:69], v[174:177], v[206:209], 0
	v_mfma_f32_16x16x32_bf16 v[118:121], v[170:173], v[186:189], v[118:121]
	v_mfma_f32_16x16x32_bf16 v[114:117], v[178:181], v[186:189], v[114:117]
	v_mfma_f32_16x16x32_bf16 v[102:105], v[170:173], v[194:197], v[102:105]
	v_mfma_f32_16x16x32_bf16 v[98:101], v[178:181], v[194:197], v[98:101]
	v_mfma_f32_16x16x32_bf16 v[86:89], v[170:173], v[202:205], v[86:89]
	v_mfma_f32_16x16x32_bf16 v[82:85], v[178:181], v[202:205], v[82:85]
	v_mfma_f32_16x16x32_bf16 v[70:73], v[170:173], v[210:213], v[70:73]
	v_mfma_f32_16x16x32_bf16 v[66:69], v[178:181], v[210:213], v[66:69]
	s_setprio 0
	s_barrier
	s_add_i32 s68, s68, s15
	v_lshl_add_u64 v[144:145], s[54:55], 0, v[166:167]
	s_mov_b32 m0, s68
	ds_read_b128 v[182:185], v149 offset:16384
	ds_read_b128 v[186:189], v149 offset:17408
	ds_read_b128 v[190:193], v149 offset:18432
	ds_read_b128 v[194:197], v149 offset:19456
	ds_read_b128 v[198:201], v149 offset:20480
	ds_read_b128 v[202:205], v149 offset:21504
	ds_read_b128 v[206:209], v149 offset:22528
	ds_read_b128 v[210:213], v149 offset:23552
	global_load_lds_dwordx4 v[144:145], off
	s_add_i32 m0, s68, 0x2000
	s_add_u32 s68, s54, 0x40000
	v_lshl_add_u64 v[214:215], s[54:55], 0, v[130:131]
	s_addc_u32 s69, s55, 0
	s_add_i32 s70, s70, s15
	global_load_lds_dwordx4 v[214:215], off
	v_lshl_add_u64 v[216:217], s[68:69], 0, v[166:167]
	s_mov_b32 m0, s70
	v_lshl_add_u64 v[218:219], s[58:59], 0, v[134:135]
	global_load_lds_dwordx4 v[216:217], off
	v_lshl_add_u64 v[216:217], s[68:69], 0, v[130:131]
	s_add_i32 m0, s70, 0x2000
	s_nop 0
	global_load_lds_dwordx4 v[216:217], off
	v_lshl_add_u64 v[216:217], s[58:59], 0, v[132:133]
	s_mov_b32 m0, s16
	s_nop 0
	global_load_lds_dwordx4 v[216:217], off
	s_mov_b32 m0, s20
	s_nop 0
	global_load_lds_dwordx4 v[218:219], off
	s_waitcnt vmcnt(8)
	s_waitcnt lgkmcnt(0)
	s_barrier
	s_setprio 1
	s_waitcnt lgkmcnt(0)
	v_mfma_f32_16x16x32_bf16 v[62:65], v[140:143], v[182:185], 0
	v_mfma_f32_16x16x32_bf16 v[58:61], v[154:157], v[182:185], 0
	v_mfma_f32_16x16x32_bf16 v[46:49], v[140:143], v[190:193], 0
	v_mfma_f32_16x16x32_bf16 v[42:45], v[154:157], v[190:193], 0
	v_mfma_f32_16x16x32_bf16 v[30:33], v[140:143], v[198:201], 0
	v_mfma_f32_16x16x32_bf16 v[26:29], v[154:157], v[198:201], 0
	v_mfma_f32_16x16x32_bf16 v[14:17], v[140:143], v[206:209], 0
	v_mfma_f32_16x16x32_bf16 v[10:13], v[154:157], v[206:209], 0
	v_mfma_f32_16x16x32_bf16 v[62:65], v[150:153], v[186:189], v[62:65]
	v_mfma_f32_16x16x32_bf16 v[58:61], v[158:161], v[186:189], v[58:61]
	v_mfma_f32_16x16x32_bf16 v[46:49], v[150:153], v[194:197], v[46:49]
	v_mfma_f32_16x16x32_bf16 v[42:45], v[158:161], v[194:197], v[42:45]
	v_mfma_f32_16x16x32_bf16 v[30:33], v[150:153], v[202:205], v[30:33]
	v_mfma_f32_16x16x32_bf16 v[26:29], v[158:161], v[202:205], v[26:29]
	v_mfma_f32_16x16x32_bf16 v[14:17], v[150:153], v[210:213], v[14:17]
	v_mfma_f32_16x16x32_bf16 v[10:13], v[158:161], v[210:213], v[10:13]
	s_setprio 0
	s_setprio 1
	v_mfma_f32_16x16x32_bf16 v[54:57], v[162:165], v[182:185], 0
	v_mfma_f32_16x16x32_bf16 v[50:53], v[174:177], v[182:185], 0
	v_mfma_f32_16x16x32_bf16 v[38:41], v[162:165], v[190:193], 0
	v_mfma_f32_16x16x32_bf16 v[34:37], v[174:177], v[190:193], 0
	v_mfma_f32_16x16x32_bf16 v[22:25], v[162:165], v[198:201], 0
	v_mfma_f32_16x16x32_bf16 v[18:21], v[174:177], v[198:201], 0
	v_mfma_f32_16x16x32_bf16 v[6:9], v[162:165], v[206:209], 0
	v_mfma_f32_16x16x32_bf16 v[2:5], v[174:177], v[206:209], 0
	v_mfma_f32_16x16x32_bf16 v[54:57], v[170:173], v[186:189], v[54:57]
	v_mfma_f32_16x16x32_bf16 v[50:53], v[178:181], v[186:189], v[50:53]
	v_mfma_f32_16x16x32_bf16 v[38:41], v[170:173], v[194:197], v[38:41]
	v_mfma_f32_16x16x32_bf16 v[34:37], v[178:181], v[194:197], v[34:37]
	v_mfma_f32_16x16x32_bf16 v[22:25], v[170:173], v[202:205], v[22:25]
	v_mfma_f32_16x16x32_bf16 v[18:21], v[178:181], v[202:205], v[18:21]
	v_mfma_f32_16x16x32_bf16 v[6:9], v[170:173], v[210:213], v[6:9]
	v_mfma_f32_16x16x32_bf16 v[2:5], v[178:181], v[210:213], v[2:5]
	s_setprio 0
	s_barrier
	s_add_i32 s68, 0, 0x18000
	s_add_i32 s69, 0, 0x1c000
	v_add_u32_e32 v158, s68, v147
	v_add_u32_e32 v169, s69, v147
	ds_read_b128 v[140:143], v158
	ds_read_b128 v[150:153], v158 offset:1024
	ds_read_b128 v[154:157], v158 offset:2048
	ds_read_b128 v[158:161], v158 offset:3072
	ds_read_b128 v[162:165], v169
	ds_read_b128 v[170:173], v169 offset:1024
	ds_read_b128 v[174:177], v169 offset:2048
	ds_read_b128 v[178:181], v169 offset:3072
	s_add_u32 s58, s58, 0x40000
	s_addc_u32 s59, s59, 0
	s_mov_b32 m0, s21
	v_lshl_add_u64 v[220:221], s[58:59], 0, v[132:133]
	ds_read_b128 v[182:185], v149 offset:32768
	ds_read_b128 v[186:189], v149 offset:33792
	ds_read_b128 v[190:193], v149 offset:34816
	ds_read_b128 v[194:197], v149 offset:35840
	ds_read_b128 v[198:201], v149 offset:36864
	ds_read_b128 v[202:205], v149 offset:37888
	ds_read_b128 v[206:209], v149 offset:38912
	ds_read_b128 v[210:213], v149 offset:39936
	global_load_lds_dwordx4 v[220:221], off
	v_lshl_add_u64 v[220:221], s[58:59], 0, v[134:135]
	s_mov_b32 m0, s22
	s_nop 0
	global_load_lds_dwordx4 v[220:221], off
	s_waitcnt vmcnt(8)
	s_waitcnt lgkmcnt(0)
	s_barrier
	s_setprio 1
	s_waitcnt lgkmcnt(0)
	v_mfma_f32_16x16x32_bf16 v[126:129], v[140:143], v[182:185], v[126:129]
	v_mfma_f32_16x16x32_bf16 v[122:125], v[154:157], v[182:185], v[122:125]
	v_mfma_f32_16x16x32_bf16 v[110:113], v[140:143], v[190:193], v[110:113]
	v_mfma_f32_16x16x32_bf16 v[106:109], v[154:157], v[190:193], v[106:109]
	v_mfma_f32_16x16x32_bf16 v[94:97], v[140:143], v[198:201], v[94:97]
	v_mfma_f32_16x16x32_bf16 v[90:93], v[154:157], v[198:201], v[90:93]
	v_mfma_f32_16x16x32_bf16 v[78:81], v[140:143], v[206:209], v[78:81]
	v_mfma_f32_16x16x32_bf16 v[74:77], v[154:157], v[206:209], v[74:77]
	v_mfma_f32_16x16x32_bf16 v[126:129], v[150:153], v[186:189], v[126:129]
	v_mfma_f32_16x16x32_bf16 v[122:125], v[158:161], v[186:189], v[122:125]
	v_mfma_f32_16x16x32_bf16 v[110:113], v[150:153], v[194:197], v[110:113]
	v_mfma_f32_16x16x32_bf16 v[106:109], v[158:161], v[194:197], v[106:109]
	v_mfma_f32_16x16x32_bf16 v[94:97], v[150:153], v[202:205], v[94:97]
	v_mfma_f32_16x16x32_bf16 v[90:93], v[158:161], v[202:205], v[90:93]
	v_mfma_f32_16x16x32_bf16 v[78:81], v[150:153], v[210:213], v[78:81]
	v_mfma_f32_16x16x32_bf16 v[74:77], v[158:161], v[210:213], v[74:77]
	s_setprio 0
	s_setprio 1
	v_mfma_f32_16x16x32_bf16 v[118:121], v[162:165], v[182:185], v[118:121]
	v_mfma_f32_16x16x32_bf16 v[114:117], v[174:177], v[182:185], v[114:117]
	v_mfma_f32_16x16x32_bf16 v[102:105], v[162:165], v[190:193], v[102:105]
	v_mfma_f32_16x16x32_bf16 v[98:101], v[174:177], v[190:193], v[98:101]
	v_mfma_f32_16x16x32_bf16 v[86:89], v[162:165], v[198:201], v[86:89]
	v_mfma_f32_16x16x32_bf16 v[82:85], v[174:177], v[198:201], v[82:85]
	v_mfma_f32_16x16x32_bf16 v[70:73], v[162:165], v[206:209], v[70:73]
	v_mfma_f32_16x16x32_bf16 v[66:69], v[174:177], v[206:209], v[66:69]
	v_mfma_f32_16x16x32_bf16 v[118:121], v[170:173], v[186:189], v[118:121]
	v_mfma_f32_16x16x32_bf16 v[114:117], v[178:181], v[186:189], v[114:117]
	v_mfma_f32_16x16x32_bf16 v[102:105], v[170:173], v[194:197], v[102:105]
	v_mfma_f32_16x16x32_bf16 v[98:101], v[178:181], v[194:197], v[98:101]
	v_mfma_f32_16x16x32_bf16 v[86:89], v[170:173], v[202:205], v[86:89]
	v_mfma_f32_16x16x32_bf16 v[82:85], v[178:181], v[202:205], v[82:85]
	v_mfma_f32_16x16x32_bf16 v[70:73], v[170:173], v[210:213], v[70:73]
	v_mfma_f32_16x16x32_bf16 v[66:69], v[178:181], v[210:213], v[66:69]
	s_setprio 0
	s_barrier
	s_add_i32 s58, s68, s15
	v_lshl_add_u64 v[144:145], v[144:145], 0, s[56:57]
	s_mov_b32 m0, s58
	ds_read_b128 v[182:185], v149 offset:49152
	ds_read_b128 v[186:189], v149 offset:50176
	ds_read_b128 v[190:193], v149 offset:51200
	ds_read_b128 v[194:197], v149 offset:52224
	ds_read_b128 v[198:201], v149 offset:53248
	ds_read_b128 v[202:205], v149 offset:54272
	ds_read_b128 v[206:209], v149 offset:55296
	ds_read_b128 v[210:213], v149 offset:56320
	global_load_lds_dwordx4 v[144:145], off
	s_add_i32 m0, s58, 0x2000
	s_add_u32 s54, s54, 0x40080
	v_lshl_add_u64 v[144:145], v[214:215], 0, s[56:57]
	s_addc_u32 s55, s55, 0
	s_add_i32 s58, s69, s15
	global_load_lds_dwordx4 v[144:145], off
	v_lshl_add_u64 v[144:145], s[54:55], 0, v[166:167]
	s_mov_b32 m0, s58
	s_nop 0
	global_load_lds_dwordx4 v[144:145], off
	v_lshl_add_u64 v[144:145], s[54:55], 0, v[130:131]
	s_add_i32 m0, s58, 0x2000
	s_nop 0
	global_load_lds_dwordx4 v[144:145], off
	v_lshl_add_u64 v[144:145], v[216:217], 0, s[56:57]
	s_mov_b32 m0, s23
	s_nop 0
	global_load_lds_dwordx4 v[144:145], off
	v_lshl_add_u64 v[144:145], v[218:219], 0, s[56:57]
	s_mov_b32 m0, s24
	s_nop 0
	global_load_lds_dwordx4 v[144:145], off
	s_waitcnt vmcnt(8)
	s_waitcnt lgkmcnt(0)
	s_barrier
	s_setprio 1
	s_waitcnt lgkmcnt(0)
	v_mfma_f32_16x16x32_bf16 v[62:65], v[140:143], v[182:185], v[62:65]
	v_mfma_f32_16x16x32_bf16 v[58:61], v[154:157], v[182:185], v[58:61]
	v_mfma_f32_16x16x32_bf16 v[46:49], v[140:143], v[190:193], v[46:49]
	v_mfma_f32_16x16x32_bf16 v[42:45], v[154:157], v[190:193], v[42:45]
	v_mfma_f32_16x16x32_bf16 v[30:33], v[140:143], v[198:201], v[30:33]
	v_mfma_f32_16x16x32_bf16 v[26:29], v[154:157], v[198:201], v[26:29]
	v_mfma_f32_16x16x32_bf16 v[14:17], v[140:143], v[206:209], v[14:17]
	v_mfma_f32_16x16x32_bf16 v[10:13], v[154:157], v[206:209], v[10:13]
	v_mfma_f32_16x16x32_bf16 v[62:65], v[150:153], v[186:189], v[62:65]
	v_mfma_f32_16x16x32_bf16 v[58:61], v[158:161], v[186:189], v[58:61]
	v_mfma_f32_16x16x32_bf16 v[46:49], v[150:153], v[194:197], v[46:49]
	v_mfma_f32_16x16x32_bf16 v[42:45], v[158:161], v[194:197], v[42:45]
	v_mfma_f32_16x16x32_bf16 v[30:33], v[150:153], v[202:205], v[30:33]
	v_mfma_f32_16x16x32_bf16 v[26:29], v[158:161], v[202:205], v[26:29]
	v_mfma_f32_16x16x32_bf16 v[14:17], v[150:153], v[210:213], v[14:17]
	v_mfma_f32_16x16x32_bf16 v[10:13], v[158:161], v[210:213], v[10:13]
	s_setprio 0
	s_setprio 1
	v_mfma_f32_16x16x32_bf16 v[54:57], v[162:165], v[182:185], v[54:57]
	v_mfma_f32_16x16x32_bf16 v[50:53], v[174:177], v[182:185], v[50:53]
	v_mfma_f32_16x16x32_bf16 v[38:41], v[162:165], v[190:193], v[38:41]
	v_mfma_f32_16x16x32_bf16 v[34:37], v[174:177], v[190:193], v[34:37]
	v_mfma_f32_16x16x32_bf16 v[22:25], v[162:165], v[198:201], v[22:25]
	v_mfma_f32_16x16x32_bf16 v[18:21], v[174:177], v[198:201], v[18:21]
	v_mfma_f32_16x16x32_bf16 v[6:9], v[162:165], v[206:209], v[6:9]
	v_mfma_f32_16x16x32_bf16 v[2:5], v[174:177], v[206:209], v[2:5]
	v_mfma_f32_16x16x32_bf16 v[54:57], v[170:173], v[186:189], v[54:57]
	v_mfma_f32_16x16x32_bf16 v[50:53], v[178:181], v[186:189], v[50:53]
	v_mfma_f32_16x16x32_bf16 v[38:41], v[170:173], v[194:197], v[38:41]
	v_mfma_f32_16x16x32_bf16 v[34:37], v[178:181], v[194:197], v[34:37]
	v_mfma_f32_16x16x32_bf16 v[22:25], v[170:173], v[202:205], v[22:25]
	v_mfma_f32_16x16x32_bf16 v[18:21], v[178:181], v[202:205], v[18:21]
	v_mfma_f32_16x16x32_bf16 v[6:9], v[170:173], v[210:213], v[6:9]
	v_mfma_f32_16x16x32_bf16 v[2:5], v[178:181], v[210:213], v[2:5]
	s_setprio 0
	s_barrier
	s_add_u32 s64, s64, 0x100
	s_addc_u32 s65, s65, 0
	s_add_u32 s52, s52, 0x100
	s_addc_u32 s53, s53, 0
	s_cmp_ge_i32 s66, s1
	s_mov_b32 s54, s66
	s_cbranch_scc0 .LBB0_1438
	s_branch .Lpeelexitph12

.Lpeelexitph12:
	s_mov_b64 s[70:71], 0xe800800
	v_mov_b32_e32 v209, v1
	s_and_b64 vcc, exec, s[34:35]
	s_cbranch_vccz .LBB0_1441

.LBB0_1776:
	v_lshl_add_u32 v250, s58, 8, v195
	v_lshlrev_b32_e32 v250, 2, v250
	global_load_dword v235, v250, s[36:37]
	global_load_dword v237, v250, s[36:37] offset:64
	global_load_dword v239, v250, s[36:37] offset:128
	global_load_dword v241, v250, s[36:37] offset:192
	global_load_dword v243, v250, s[36:37] offset:512
	global_load_dword v245, v250, s[36:37] offset:576
	global_load_dword v247, v250, s[36:37] offset:640
	global_load_dword v249, v250, s[36:37] offset:704
	global_load_dword v234, v250, s[40:41]
	global_load_dword v236, v250, s[40:41] offset:64
	global_load_dword v238, v250, s[40:41] offset:128
	global_load_dword v240, v250, s[40:41] offset:192
	global_load_dword v242, v250, s[40:41] offset:512
	global_load_dword v244, v250, s[40:41] offset:576
	global_load_dword v246, v250, s[40:41] offset:640
	global_load_dword v248, v250, s[40:41] offset:704
	s_add_u32 s51, s62, 0x100
	v_mov_b32_e32 v1, 0x3ecc95a3
	s_addc_u32 s59, s63, 0
	s_mov_b32 s64, 0
.Lpeelph16_0:
	s_add_i32 s91, s64, 2
	s_add_u32 s62, s60, 0x100
	s_addc_u32 s63, s61, 0
	s_add_i32 s92, 0, 0x10000
	s_cmp_eq_u32 s74, s64
	s_cselect_b32 s69, s53, s63
	s_cselect_b32 s68, s52, s62
	s_cselect_b32 s65, s55, s59
	s_cselect_b32 s64, s54, s51
	s_add_i32 s93, 0, 0x14000
	v_add_u32_e32 v2, s92, v196
	v_add_u32_e32 v6, s93, v196
	ds_read_b128 v[26:29], v2
	ds_read_b128 v[30:33], v2 offset:1024
	ds_read_b128 v[18:21], v2 offset:2048
	ds_read_b128 v[22:25], v2 offset:3072
	ds_read_b128 v[10:13], v6
	ds_read_b128 v[14:17], v6 offset:1024
	ds_read_b128 v[2:5], v6 offset:2048
	ds_read_b128 v[6:9], v6 offset:3072
	v_lshl_add_u64 v[216:217], s[60:61], 0, v[184:185]
	s_add_i32 m0, s21, 0xc000
	ds_read_b128 v[170:173], v198
	ds_read_b128 v[174:177], v198 offset:1024
	ds_read_b128 v[186:189], v198 offset:2048
	ds_read_b128 v[190:193], v198 offset:3072
	ds_read_b128 v[200:203], v198 offset:4096
	ds_read_b128 v[204:207], v198 offset:5120
	ds_read_b128 v[208:211], v198 offset:6144
	ds_read_b128 v[212:215], v198 offset:7168
	global_load_lds_dwordx4 v[216:217], off
	v_lshl_add_u64 v[216:217], s[60:61], 0, v[182:183]
	s_add_i32 m0, s21, 0xe000
	s_nop 0
	global_load_lds_dwordx4 v[216:217], off
	s_waitcnt vmcnt(8)
	s_waitcnt lgkmcnt(0)
	s_barrier
	s_setprio 1
	s_waitcnt lgkmcnt(0)
	v_mfma_scale_f32_16x16x128_f8f6f4 v[154:157], v[26:33], v[170:177], 0, v194, v169 op_sel_hi:[0,0,0]
	v_mfma_scale_f32_16x16x128_f8f6f4 v[158:161], v[18:25], v[170:177], 0, v194, v169 op_sel_hi:[0,0,0]
	v_mfma_scale_f32_16x16x128_f8f6f4 v[138:141], v[26:33], v[186:193], 0, v194, v169 op_sel_hi:[0,0,0]
	v_mfma_scale_f32_16x16x128_f8f6f4 v[142:145], v[18:25], v[186:193], 0, v194, v169 op_sel_hi:[0,0,0]
	v_mfma_scale_f32_16x16x128_f8f6f4 v[122:125], v[26:33], v[200:207], 0, v194, v169 op_sel_hi:[0,0,0]
	v_mfma_scale_f32_16x16x128_f8f6f4 v[126:129], v[18:25], v[200:207], 0, v194, v169 op_sel_hi:[0,0,0]
	v_mfma_scale_f32_16x16x128_f8f6f4 v[106:109], v[26:33], v[208:215], 0, v194, v169 op_sel_hi:[0,0,0]
	v_mfma_scale_f32_16x16x128_f8f6f4 v[110:113], v[18:25], v[208:215], 0, v194, v169 op_sel_hi:[0,0,0]
	s_setprio 0
	s_setprio 1
	v_mfma_scale_f32_16x16x128_f8f6f4 v[146:149], v[10:17], v[170:177], 0, v194, v169 op_sel_hi:[0,0,0]
	v_mfma_scale_f32_16x16x128_f8f6f4 v[150:153], v[2:9], v[170:177], 0, v194, v169 op_sel_hi:[0,0,0]
	v_mfma_scale_f32_16x16x128_f8f6f4 v[130:133], v[10:17], v[186:193], 0, v194, v169 op_sel_hi:[0,0,0]
	v_mfma_scale_f32_16x16x128_f8f6f4 v[134:137], v[2:9], v[186:193], 0, v194, v169 op_sel_hi:[0,0,0]
	v_mfma_scale_f32_16x16x128_f8f6f4 v[114:117], v[10:17], v[200:207], 0, v194, v169 op_sel_hi:[0,0,0]
	v_mfma_scale_f32_16x16x128_f8f6f4 v[118:121], v[2:9], v[200:207], 0, v194, v169 op_sel_hi:[0,0,0]
	v_mfma_scale_f32_16x16x128_f8f6f4 v[98:101], v[10:17], v[208:215], 0, v194, v169 op_sel_hi:[0,0,0]
	v_mfma_scale_f32_16x16x128_f8f6f4 v[102:105], v[2:9], v[208:215], 0, v194, v169 op_sel_hi:[0,0,0]
	s_setprio 0
	s_barrier
	s_add_i32 s60, s92, s20
	v_lshl_add_u64 v[186:187], s[64:65], 0, v[164:165]
	s_mov_b32 m0, s60
	ds_read_b128 v[170:173], v198 offset:16384
	ds_read_b128 v[174:177], v198 offset:17408
	ds_read_b128 v[200:203], v198 offset:18432
	ds_read_b128 v[204:207], v198 offset:19456
	ds_read_b128 v[208:211], v198 offset:20480
	ds_read_b128 v[212:215], v198 offset:21504
	ds_read_b128 v[216:219], v198 offset:22528
	ds_read_b128 v[220:223], v198 offset:23552
	global_load_lds_dwordx4 v[186:187], off
	s_add_i32 m0, s60, 0x2000
	s_add_u32 s60, s64, 0x70000
	v_lshl_add_u64 v[188:189], s[64:65], 0, v[180:181]
	s_addc_u32 s61, s65, 0
	s_add_i32 s92, s93, s20
	global_load_lds_dwordx4 v[188:189], off
	v_lshl_add_u64 v[190:191], s[60:61], 0, v[164:165]
	s_mov_b32 m0, s92
	v_lshl_add_u64 v[192:193], s[68:69], 0, v[178:179]
	global_load_lds_dwordx4 v[190:191], off
	v_lshl_add_u64 v[190:191], s[60:61], 0, v[180:181]
	s_add_i32 m0, s92, 0x2000
	s_nop 0
	global_load_lds_dwordx4 v[190:191], off
	v_lshl_add_u64 v[190:191], s[68:69], 0, v[162:163]
	s_mov_b32 m0, s21
	s_nop 0
	global_load_lds_dwordx4 v[190:191], off
	s_mov_b32 m0, s22
	s_nop 0
	global_load_lds_dwordx4 v[192:193], off
	s_waitcnt vmcnt(8)
	s_waitcnt lgkmcnt(0)
	s_barrier
	s_setprio 1
	s_waitcnt lgkmcnt(0)
	v_mfma_scale_f32_16x16x128_f8f6f4 v[90:93], v[26:33], v[170:177], 0, v194, v169 op_sel_hi:[0,0,0]
	v_mfma_scale_f32_16x16x128_f8f6f4 v[94:97], v[18:25], v[170:177], 0, v194, v169 op_sel_hi:[0,0,0]
	v_mfma_scale_f32_16x16x128_f8f6f4 v[74:77], v[26:33], v[200:207], 0, v194, v169 op_sel_hi:[0,0,0]
	v_mfma_scale_f32_16x16x128_f8f6f4 v[78:81], v[18:25], v[200:207], 0, v194, v169 op_sel_hi:[0,0,0]
	v_mfma_scale_f32_16x16x128_f8f6f4 v[58:61], v[26:33], v[208:215], 0, v194, v169 op_sel_hi:[0,0,0]
	v_mfma_scale_f32_16x16x128_f8f6f4 v[62:65], v[18:25], v[208:215], 0, v194, v169 op_sel_hi:[0,0,0]
	v_mfma_scale_f32_16x16x128_f8f6f4 v[42:45], v[26:33], v[216:223], 0, v194, v169 op_sel_hi:[0,0,0]
	v_mfma_scale_f32_16x16x128_f8f6f4 v[46:49], v[18:25], v[216:223], 0, v194, v169 op_sel_hi:[0,0,0]
	s_setprio 0
	s_setprio 1
	v_mfma_scale_f32_16x16x128_f8f6f4 v[82:85], v[10:17], v[170:177], 0, v194, v169 op_sel_hi:[0,0,0]
	v_mfma_scale_f32_16x16x128_f8f6f4 v[86:89], v[2:9], v[170:177], 0, v194, v169 op_sel_hi:[0,0,0]
	v_mfma_scale_f32_16x16x128_f8f6f4 v[66:69], v[10:17], v[200:207], 0, v194, v169 op_sel_hi:[0,0,0]
	v_mfma_scale_f32_16x16x128_f8f6f4 v[70:73], v[2:9], v[200:207], 0, v194, v169 op_sel_hi:[0,0,0]
	v_mfma_scale_f32_16x16x128_f8f6f4 v[50:53], v[10:17], v[208:215], 0, v194, v169 op_sel_hi:[0,0,0]
	v_mfma_scale_f32_16x16x128_f8f6f4 v[54:57], v[2:9], v[208:215], 0, v194, v169 op_sel_hi:[0,0,0]
	v_mfma_scale_f32_16x16x128_f8f6f4 v[34:37], v[10:17], v[216:223], 0, v194, v169 op_sel_hi:[0,0,0]
	v_mfma_scale_f32_16x16x128_f8f6f4 v[38:41], v[2:9], v[216:223], 0, v194, v169 op_sel_hi:[0,0,0]
	s_setprio 0
	s_barrier
	s_add_i32 s92, 0, 0x18000
	s_add_i32 s93, 0, 0x1c000
	v_add_u32_e32 v2, s92, v196
	v_add_u32_e32 v6, s93, v196
	ds_read_b128 v[26:29], v2
	ds_read_b128 v[30:33], v2 offset:1024
	ds_read_b128 v[18:21], v2 offset:2048
	ds_read_b128 v[22:25], v2 offset:3072
	ds_read_b128 v[10:13], v6
	ds_read_b128 v[14:17], v6 offset:1024
	ds_read_b128 v[2:5], v6 offset:2048
	ds_read_b128 v[6:9], v6 offset:3072
	s_add_u32 s60, s68, 0x70000
	s_addc_u32 s61, s69, 0
	s_mov_b32 m0, s23
	v_lshl_add_u64 v[232:233], s[60:61], 0, v[162:163]
	ds_read_b128 v[170:173], v198 offset:32768
	ds_read_b128 v[174:177], v198 offset:33792
	ds_read_b128 v[200:203], v198 offset:34816
	ds_read_b128 v[204:207], v198 offset:35840
	ds_read_b128 v[208:211], v198 offset:36864
	ds_read_b128 v[212:215], v198 offset:37888
	ds_read_b128 v[216:219], v198 offset:38912
	ds_read_b128 v[220:223], v198 offset:39936
	global_load_lds_dwordx4 v[232:233], off
	v_lshl_add_u64 v[232:233], s[60:61], 0, v[178:179]
	s_mov_b32 m0, s70
	s_nop 0
	global_load_lds_dwordx4 v[232:233], off
	s_waitcnt vmcnt(8)
	s_waitcnt lgkmcnt(0)
	s_barrier
	s_setprio 1
	s_waitcnt lgkmcnt(0)
	v_mfma_scale_f32_16x16x128_f8f6f4 v[154:157], v[26:33], v[170:177], v[154:157], v194, v169 op_sel_hi:[0,0,0]
	v_mfma_scale_f32_16x16x128_f8f6f4 v[158:161], v[18:25], v[170:177], v[158:161], v194, v169 op_sel_hi:[0,0,0]
	v_mfma_scale_f32_16x16x128_f8f6f4 v[138:141], v[26:33], v[200:207], v[138:141], v194, v169 op_sel_hi:[0,0,0]
	v_mfma_scale_f32_16x16x128_f8f6f4 v[142:145], v[18:25], v[200:207], v[142:145], v194, v169 op_sel_hi:[0,0,0]
	v_mfma_scale_f32_16x16x128_f8f6f4 v[122:125], v[26:33], v[208:215], v[122:125], v194, v169 op_sel_hi:[0,0,0]
	v_mfma_scale_f32_16x16x128_f8f6f4 v[126:129], v[18:25], v[208:215], v[126:129], v194, v169 op_sel_hi:[0,0,0]
	v_mfma_scale_f32_16x16x128_f8f6f4 v[106:109], v[26:33], v[216:223], v[106:109], v194, v169 op_sel_hi:[0,0,0]
	v_mfma_scale_f32_16x16x128_f8f6f4 v[110:113], v[18:25], v[216:223], v[110:113], v194, v169 op_sel_hi:[0,0,0]
	s_setprio 0
	s_setprio 1
	v_mfma_scale_f32_16x16x128_f8f6f4 v[146:149], v[10:17], v[170:177], v[146:149], v194, v169 op_sel_hi:[0,0,0]
	v_mfma_scale_f32_16x16x128_f8f6f4 v[150:153], v[2:9], v[170:177], v[150:153], v194, v169 op_sel_hi:[0,0,0]
	v_mfma_scale_f32_16x16x128_f8f6f4 v[130:133], v[10:17], v[200:207], v[130:133], v194, v169 op_sel_hi:[0,0,0]
	v_mfma_scale_f32_16x16x128_f8f6f4 v[134:137], v[2:9], v[200:207], v[134:137], v194, v169 op_sel_hi:[0,0,0]
	v_mfma_scale_f32_16x16x128_f8f6f4 v[114:117], v[10:17], v[208:215], v[114:117], v194, v169 op_sel_hi:[0,0,0]
	v_mfma_scale_f32_16x16x128_f8f6f4 v[118:121], v[2:9], v[208:215], v[118:121], v194, v169 op_sel_hi:[0,0,0]
	v_mfma_scale_f32_16x16x128_f8f6f4 v[98:101], v[10:17], v[216:223], v[98:101], v194, v169 op_sel_hi:[0,0,0]
	v_mfma_scale_f32_16x16x128_f8f6f4 v[102:105], v[2:9], v[216:223], v[102:105], v194, v169 op_sel_hi:[0,0,0]
	s_setprio 0
	s_barrier
	s_add_i32 s60, s92, s20
	v_lshl_add_u64 v[186:187], v[186:187], 0, s[56:57]
	s_mov_b32 m0, s60
	ds_read_b128 v[170:173], v198 offset:49152
	ds_read_b128 v[174:177], v198 offset:50176
	ds_read_b128 v[200:203], v198 offset:51200
	ds_read_b128 v[204:207], v198 offset:52224
	ds_read_b128 v[208:211], v198 offset:53248
	ds_read_b128 v[212:215], v198 offset:54272
	ds_read_b128 v[216:219], v198 offset:55296
	ds_read_b128 v[220:223], v198 offset:56320
	global_load_lds_dwordx4 v[186:187], off
	s_add_i32 m0, s60, 0x2000
	s_add_u32 s60, s64, 0x70080
	v_lshl_add_u64 v[186:187], v[188:189], 0, s[56:57]
	s_addc_u32 s61, s65, 0
	s_add_i32 s64, s93, s20
	global_load_lds_dwordx4 v[186:187], off
	v_lshl_add_u64 v[186:187], s[60:61], 0, v[164:165]
	s_mov_b32 m0, s64
	s_nop 0
	global_load_lds_dwordx4 v[186:187], off
	v_lshl_add_u64 v[186:187], s[60:61], 0, v[180:181]
	s_add_i32 m0, s64, 0x2000
	s_nop 0
	global_load_lds_dwordx4 v[186:187], off
	v_lshl_add_u64 v[186:187], v[190:191], 0, s[56:57]
	s_mov_b32 m0, s71
	s_nop 0
	global_load_lds_dwordx4 v[186:187], off
	v_lshl_add_u64 v[186:187], v[192:193], 0, s[56:57]
	s_mov_b32 m0, s72
	s_nop 0
	global_load_lds_dwordx4 v[186:187], off
	s_waitcnt vmcnt(8)
	s_waitcnt lgkmcnt(0)
	s_barrier
	s_setprio 1
	s_waitcnt lgkmcnt(0)
	v_mfma_scale_f32_16x16x128_f8f6f4 v[90:93], v[26:33], v[170:177], v[90:93], v194, v169 op_sel_hi:[0,0,0]
	v_mfma_scale_f32_16x16x128_f8f6f4 v[94:97], v[18:25], v[170:177], v[94:97], v194, v169 op_sel_hi:[0,0,0]
	v_mfma_scale_f32_16x16x128_f8f6f4 v[74:77], v[26:33], v[200:207], v[74:77], v194, v169 op_sel_hi:[0,0,0]
	v_mfma_scale_f32_16x16x128_f8f6f4 v[78:81], v[18:25], v[200:207], v[78:81], v194, v169 op_sel_hi:[0,0,0]
	v_mfma_scale_f32_16x16x128_f8f6f4 v[58:61], v[26:33], v[208:215], v[58:61], v194, v169 op_sel_hi:[0,0,0]
	v_mfma_scale_f32_16x16x128_f8f6f4 v[62:65], v[18:25], v[208:215], v[62:65], v194, v169 op_sel_hi:[0,0,0]
	v_mfma_scale_f32_16x16x128_f8f6f4 v[42:45], v[26:33], v[216:223], v[42:45], v194, v169 op_sel_hi:[0,0,0]
	v_mfma_scale_f32_16x16x128_f8f6f4 v[46:49], v[18:25], v[216:223], v[46:49], v194, v169 op_sel_hi:[0,0,0]
	s_setprio 0
	s_setprio 1
	v_mfma_scale_f32_16x16x128_f8f6f4 v[82:85], v[10:17], v[170:177], v[82:85], v194, v169 op_sel_hi:[0,0,0]
	v_mfma_scale_f32_16x16x128_f8f6f4 v[86:89], v[2:9], v[170:177], v[86:89], v194, v169 op_sel_hi:[0,0,0]
	v_mfma_scale_f32_16x16x128_f8f6f4 v[66:69], v[10:17], v[200:207], v[66:69], v194, v169 op_sel_hi:[0,0,0]
	v_mfma_scale_f32_16x16x128_f8f6f4 v[70:73], v[2:9], v[200:207], v[70:73], v194, v169 op_sel_hi:[0,0,0]
	v_mfma_scale_f32_16x16x128_f8f6f4 v[50:53], v[10:17], v[208:215], v[50:53], v194, v169 op_sel_hi:[0,0,0]
	v_mfma_scale_f32_16x16x128_f8f6f4 v[54:57], v[2:9], v[208:215], v[54:57], v194, v169 op_sel_hi:[0,0,0]
	v_mfma_scale_f32_16x16x128_f8f6f4 v[34:37], v[10:17], v[216:223], v[34:37], v194, v169 op_sel_hi:[0,0,0]
	v_mfma_scale_f32_16x16x128_f8f6f4 v[38:41], v[2:9], v[216:223], v[38:41], v194, v169 op_sel_hi:[0,0,0]
	s_setprio 0
	s_barrier
	s_add_u32 s51, s51, 0x100
	s_addc_u32 s59, s59, 0
	s_cmp_ge_i32 s91, s8
	s_mov_b64 s[60:61], s[62:63]
	s_mov_b32 s64, s91
	s_cbranch_scc0 .LBB0_1777
	s_branch .Lpeelexitph16

.Lpeelexitph16:
	s_movk_i32 s93, 0x1000
	v_mov_b32_e32 v209, v1
	s_and_b64 vcc, exec, s[44:45]
	s_cbranch_vccz .LBB0_1780

.LBB0_1922:
	s_add_u32 s35, s70, 0x100
	v_mov_b32_e32 v1, 0x3ecc95a3
	s_addc_u32 s45, s71, 0
	s_mov_b32 s70, 0
.Lpeelph18_0:
	s_add_i32 s75, s70, 2
	s_add_u32 s42, s18, 0x100
	s_addc_u32 s43, s19, 0
	s_add_i32 s46, 0, 0x10000
	s_cmp_eq_u32 s14, s70
	s_cselect_b32 vcc_hi, s69, s43
	s_cselect_b32 vcc_lo, s68, s42
	s_cselect_b32 s71, s37, s45
	s_cselect_b32 s70, s36, s35
	s_add_i32 s47, 0, 0x14000
	v_add_u32_e32 v2, s46, v196
	v_add_u32_e32 v6, s47, v196
	ds_read_b128 v[26:29], v2
	ds_read_b128 v[30:33], v2 offset:1024
	ds_read_b128 v[18:21], v2 offset:2048
	ds_read_b128 v[22:25], v2 offset:3072
	ds_read_b128 v[10:13], v6
	ds_read_b128 v[14:17], v6 offset:1024
	ds_read_b128 v[2:5], v6 offset:2048
	ds_read_b128 v[6:9], v6 offset:3072
	v_lshl_add_u64 v[218:219], s[18:19], 0, v[184:185]
	s_add_i32 m0, s73, 0xc000
	ds_read_b128 v[170:173], v201
	ds_read_b128 v[174:177], v201 offset:1024
	ds_read_b128 v[186:189], v201 offset:2048
	ds_read_b128 v[190:193], v201 offset:3072
	ds_read_b128 v[202:205], v201 offset:4096
	ds_read_b128 v[206:209], v201 offset:5120
	ds_read_b128 v[210:213], v201 offset:6144
	ds_read_b128 v[214:217], v201 offset:7168
	global_load_lds_dwordx4 v[218:219], off
	v_lshl_add_u64 v[218:219], s[18:19], 0, v[182:183]
	s_add_i32 m0, s73, 0xe000
	s_nop 0
	global_load_lds_dwordx4 v[218:219], off
	s_waitcnt vmcnt(8)
	s_waitcnt lgkmcnt(0)
	s_barrier
	s_setprio 1
	s_waitcnt lgkmcnt(0)
	v_mfma_scale_f32_16x16x128_f8f6f4 v[158:161], v[26:33], v[170:177], 0, v194, v169 op_sel_hi:[0,0,0]
	v_mfma_scale_f32_16x16x128_f8f6f4 v[154:157], v[18:25], v[170:177], 0, v194, v169 op_sel_hi:[0,0,0]
	v_mfma_scale_f32_16x16x128_f8f6f4 v[142:145], v[26:33], v[186:193], 0, v194, v169 op_sel_hi:[0,0,0]
	v_mfma_scale_f32_16x16x128_f8f6f4 v[138:141], v[18:25], v[186:193], 0, v194, v169 op_sel_hi:[0,0,0]
	v_mfma_scale_f32_16x16x128_f8f6f4 v[126:129], v[26:33], v[202:209], 0, v194, v169 op_sel_hi:[0,0,0]
	v_mfma_scale_f32_16x16x128_f8f6f4 v[122:125], v[18:25], v[202:209], 0, v194, v169 op_sel_hi:[0,0,0]
	v_mfma_scale_f32_16x16x128_f8f6f4 v[110:113], v[26:33], v[210:217], 0, v194, v169 op_sel_hi:[0,0,0]
	v_mfma_scale_f32_16x16x128_f8f6f4 v[106:109], v[18:25], v[210:217], 0, v194, v169 op_sel_hi:[0,0,0]
	s_setprio 0
	s_setprio 1
	v_mfma_scale_f32_16x16x128_f8f6f4 v[150:153], v[10:17], v[170:177], 0, v194, v169 op_sel_hi:[0,0,0]
	v_mfma_scale_f32_16x16x128_f8f6f4 v[146:149], v[2:9], v[170:177], 0, v194, v169 op_sel_hi:[0,0,0]
	v_mfma_scale_f32_16x16x128_f8f6f4 v[134:137], v[10:17], v[186:193], 0, v194, v169 op_sel_hi:[0,0,0]
	v_mfma_scale_f32_16x16x128_f8f6f4 v[130:133], v[2:9], v[186:193], 0, v194, v169 op_sel_hi:[0,0,0]
	v_mfma_scale_f32_16x16x128_f8f6f4 v[118:121], v[10:17], v[202:209], 0, v194, v169 op_sel_hi:[0,0,0]
	v_mfma_scale_f32_16x16x128_f8f6f4 v[114:117], v[2:9], v[202:209], 0, v194, v169 op_sel_hi:[0,0,0]
	v_mfma_scale_f32_16x16x128_f8f6f4 v[102:105], v[10:17], v[210:217], 0, v194, v169 op_sel_hi:[0,0,0]
	v_mfma_scale_f32_16x16x128_f8f6f4 v[98:101], v[2:9], v[210:217], 0, v194, v169 op_sel_hi:[0,0,0]
	s_setprio 0
	s_barrier
	s_add_i32 s18, s46, s95
	v_lshl_add_u64 v[186:187], s[70:71], 0, v[164:165]
	s_mov_b32 m0, s18
	ds_read_b128 v[170:173], v201 offset:16384
	ds_read_b128 v[174:177], v201 offset:17408
	ds_read_b128 v[202:205], v201 offset:18432
	ds_read_b128 v[206:209], v201 offset:19456
	ds_read_b128 v[210:213], v201 offset:20480
	ds_read_b128 v[214:217], v201 offset:21504
	ds_read_b128 v[236:239], v201 offset:22528
	ds_read_b128 v[240:243], v201 offset:23552
	global_load_lds_dwordx4 v[186:187], off
	s_add_i32 m0, s18, 0x2000
	s_add_u32 s18, s70, 0x70000
	v_lshl_add_u64 v[188:189], s[70:71], 0, v[180:181]
	s_addc_u32 s19, s71, 0
	s_add_i32 s46, s47, s95
	global_load_lds_dwordx4 v[188:189], off
	v_lshl_add_u64 v[190:191], s[18:19], 0, v[164:165]
	s_mov_b32 m0, s46
	v_lshl_add_u64 v[192:193], vcc, 0, v[178:179]
	global_load_lds_dwordx4 v[190:191], off
	v_lshl_add_u64 v[190:191], s[18:19], 0, v[180:181]
	s_add_i32 m0, s46, 0x2000
	s_nop 0
	global_load_lds_dwordx4 v[190:191], off
	v_lshl_add_u64 v[190:191], vcc, 0, v[162:163]
	s_mov_b32 m0, s73
	s_nop 0
	global_load_lds_dwordx4 v[190:191], off
	s_mov_b32 m0, s8
	s_nop 0
	global_load_lds_dwordx4 v[192:193], off
	s_waitcnt vmcnt(8)
	s_waitcnt lgkmcnt(0)
	s_barrier
	s_setprio 1
	s_waitcnt lgkmcnt(0)
	v_mfma_scale_f32_16x16x128_f8f6f4 v[94:97], v[26:33], v[170:177], 0, v194, v169 op_sel_hi:[0,0,0]
	v_mfma_scale_f32_16x16x128_f8f6f4 v[90:93], v[18:25], v[170:177], 0, v194, v169 op_sel_hi:[0,0,0]
	v_mfma_scale_f32_16x16x128_f8f6f4 v[78:81], v[26:33], v[202:209], 0, v194, v169 op_sel_hi:[0,0,0]
	v_mfma_scale_f32_16x16x128_f8f6f4 v[74:77], v[18:25], v[202:209], 0, v194, v169 op_sel_hi:[0,0,0]
	v_mfma_scale_f32_16x16x128_f8f6f4 v[62:65], v[26:33], v[210:217], 0, v194, v169 op_sel_hi:[0,0,0]
	v_mfma_scale_f32_16x16x128_f8f6f4 v[58:61], v[18:25], v[210:217], 0, v194, v169 op_sel_hi:[0,0,0]
	v_mfma_scale_f32_16x16x128_f8f6f4 v[46:49], v[26:33], v[236:243], 0, v194, v169 op_sel_hi:[0,0,0]
	v_mfma_scale_f32_16x16x128_f8f6f4 v[42:45], v[18:25], v[236:243], 0, v194, v169 op_sel_hi:[0,0,0]
	s_setprio 0
	s_setprio 1
	v_mfma_scale_f32_16x16x128_f8f6f4 v[86:89], v[10:17], v[170:177], 0, v194, v169 op_sel_hi:[0,0,0]
	v_mfma_scale_f32_16x16x128_f8f6f4 v[82:85], v[2:9], v[170:177], 0, v194, v169 op_sel_hi:[0,0,0]
	v_mfma_scale_f32_16x16x128_f8f6f4 v[70:73], v[10:17], v[202:209], 0, v194, v169 op_sel_hi:[0,0,0]
	v_mfma_scale_f32_16x16x128_f8f6f4 v[66:69], v[2:9], v[202:209], 0, v194, v169 op_sel_hi:[0,0,0]
	v_mfma_scale_f32_16x16x128_f8f6f4 v[54:57], v[10:17], v[210:217], 0, v194, v169 op_sel_hi:[0,0,0]
	v_mfma_scale_f32_16x16x128_f8f6f4 v[50:53], v[2:9], v[210:217], 0, v194, v169 op_sel_hi:[0,0,0]
	v_mfma_scale_f32_16x16x128_f8f6f4 v[38:41], v[10:17], v[236:243], 0, v194, v169 op_sel_hi:[0,0,0]
	v_mfma_scale_f32_16x16x128_f8f6f4 v[34:37], v[2:9], v[236:243], 0, v194, v169 op_sel_hi:[0,0,0]
	s_setprio 0
	s_barrier
	s_add_i32 s46, 0, 0x18000
	s_add_i32 s47, 0, 0x1c000
	v_add_u32_e32 v2, s46, v196
	v_add_u32_e32 v6, s47, v196
	ds_read_b128 v[26:29], v2
	ds_read_b128 v[30:33], v2 offset:1024
	ds_read_b128 v[18:21], v2 offset:2048
	ds_read_b128 v[22:25], v2 offset:3072
	ds_read_b128 v[10:13], v6
	ds_read_b128 v[14:17], v6 offset:1024
	ds_read_b128 v[2:5], v6 offset:2048
	ds_read_b128 v[6:9], v6 offset:3072
	s_add_u32 s18, vcc_lo, 0x70000
	s_addc_u32 s19, vcc_hi, 0
	s_mov_b32 m0, s11
	v_lshl_add_u64 v[218:219], s[18:19], 0, v[162:163]
	ds_read_b128 v[170:173], v201 offset:32768
	ds_read_b128 v[174:177], v201 offset:33792
	ds_read_b128 v[202:205], v201 offset:34816
	ds_read_b128 v[206:209], v201 offset:35840
	ds_read_b128 v[210:213], v201 offset:36864
	ds_read_b128 v[214:217], v201 offset:37888
	ds_read_b128 v[236:239], v201 offset:38912
	ds_read_b128 v[240:243], v201 offset:39936
	global_load_lds_dwordx4 v[218:219], off
	v_lshl_add_u64 v[218:219], s[18:19], 0, v[178:179]
	s_mov_b32 m0, s84
	s_nop 0
	global_load_lds_dwordx4 v[218:219], off
	s_waitcnt vmcnt(8)
	s_waitcnt lgkmcnt(0)
	s_barrier
	s_setprio 1
	s_waitcnt lgkmcnt(0)
	v_mfma_scale_f32_16x16x128_f8f6f4 v[158:161], v[26:33], v[170:177], v[158:161], v194, v169 op_sel_hi:[0,0,0]
	v_mfma_scale_f32_16x16x128_f8f6f4 v[154:157], v[18:25], v[170:177], v[154:157], v194, v169 op_sel_hi:[0,0,0]
	v_mfma_scale_f32_16x16x128_f8f6f4 v[142:145], v[26:33], v[202:209], v[142:145], v194, v169 op_sel_hi:[0,0,0]
	v_mfma_scale_f32_16x16x128_f8f6f4 v[138:141], v[18:25], v[202:209], v[138:141], v194, v169 op_sel_hi:[0,0,0]
	v_mfma_scale_f32_16x16x128_f8f6f4 v[126:129], v[26:33], v[210:217], v[126:129], v194, v169 op_sel_hi:[0,0,0]
	v_mfma_scale_f32_16x16x128_f8f6f4 v[122:125], v[18:25], v[210:217], v[122:125], v194, v169 op_sel_hi:[0,0,0]
	v_mfma_scale_f32_16x16x128_f8f6f4 v[110:113], v[26:33], v[236:243], v[110:113], v194, v169 op_sel_hi:[0,0,0]
	v_mfma_scale_f32_16x16x128_f8f6f4 v[106:109], v[18:25], v[236:243], v[106:109], v194, v169 op_sel_hi:[0,0,0]
	s_setprio 0
	s_setprio 1
	v_mfma_scale_f32_16x16x128_f8f6f4 v[150:153], v[10:17], v[170:177], v[150:153], v194, v169 op_sel_hi:[0,0,0]
	v_mfma_scale_f32_16x16x128_f8f6f4 v[146:149], v[2:9], v[170:177], v[146:149], v194, v169 op_sel_hi:[0,0,0]
	v_mfma_scale_f32_16x16x128_f8f6f4 v[134:137], v[10:17], v[202:209], v[134:137], v194, v169 op_sel_hi:[0,0,0]
	v_mfma_scale_f32_16x16x128_f8f6f4 v[130:133], v[2:9], v[202:209], v[130:133], v194, v169 op_sel_hi:[0,0,0]
	v_mfma_scale_f32_16x16x128_f8f6f4 v[118:121], v[10:17], v[210:217], v[118:121], v194, v169 op_sel_hi:[0,0,0]
	v_mfma_scale_f32_16x16x128_f8f6f4 v[114:117], v[2:9], v[210:217], v[114:117], v194, v169 op_sel_hi:[0,0,0]
	v_mfma_scale_f32_16x16x128_f8f6f4 v[102:105], v[10:17], v[236:243], v[102:105], v194, v169 op_sel_hi:[0,0,0]
	v_mfma_scale_f32_16x16x128_f8f6f4 v[98:101], v[2:9], v[236:243], v[98:101], v194, v169 op_sel_hi:[0,0,0]
	s_setprio 0
	s_barrier
	s_add_i32 s18, s46, s95
	v_lshl_add_u64 v[186:187], v[186:187], 0, s[56:57]
	s_mov_b32 m0, s18
	ds_read_b128 v[170:173], v201 offset:49152
	ds_read_b128 v[174:177], v201 offset:50176
	ds_read_b128 v[202:205], v201 offset:51200
	ds_read_b128 v[206:209], v201 offset:52224
	ds_read_b128 v[210:213], v201 offset:53248
	ds_read_b128 v[214:217], v201 offset:54272
	ds_read_b128 v[236:239], v201 offset:55296
	ds_read_b128 v[240:243], v201 offset:56320
	global_load_lds_dwordx4 v[186:187], off
	s_add_i32 m0, s18, 0x2000
	s_add_u32 s18, s70, 0x70080
	v_lshl_add_u64 v[186:187], v[188:189], 0, s[56:57]
	s_addc_u32 s19, s71, 0
	s_add_i32 s46, s47, s95
	global_load_lds_dwordx4 v[186:187], off
	v_lshl_add_u64 v[186:187], s[18:19], 0, v[164:165]
	s_mov_b32 m0, s46
	s_nop 0
	global_load_lds_dwordx4 v[186:187], off
	v_lshl_add_u64 v[186:187], s[18:19], 0, v[180:181]
	s_add_i32 m0, s46, 0x2000
	s_nop 0
	global_load_lds_dwordx4 v[186:187], off
	v_lshl_add_u64 v[186:187], v[190:191], 0, s[56:57]
	s_mov_b32 m0, s0
	s_nop 0
	global_load_lds_dwordx4 v[186:187], off
	v_lshl_add_u64 v[186:187], v[192:193], 0, s[56:57]
	s_mov_b32 m0, s88
	s_nop 0
	global_load_lds_dwordx4 v[186:187], off
	s_waitcnt vmcnt(8)
	s_waitcnt lgkmcnt(0)
	s_barrier
	s_setprio 1
	s_waitcnt lgkmcnt(0)
	v_mfma_scale_f32_16x16x128_f8f6f4 v[94:97], v[26:33], v[170:177], v[94:97], v194, v169 op_sel_hi:[0,0,0]
	v_mfma_scale_f32_16x16x128_f8f6f4 v[90:93], v[18:25], v[170:177], v[90:93], v194, v169 op_sel_hi:[0,0,0]
	v_mfma_scale_f32_16x16x128_f8f6f4 v[78:81], v[26:33], v[202:209], v[78:81], v194, v169 op_sel_hi:[0,0,0]
	v_mfma_scale_f32_16x16x128_f8f6f4 v[74:77], v[18:25], v[202:209], v[74:77], v194, v169 op_sel_hi:[0,0,0]
	v_mfma_scale_f32_16x16x128_f8f6f4 v[62:65], v[26:33], v[210:217], v[62:65], v194, v169 op_sel_hi:[0,0,0]
	v_mfma_scale_f32_16x16x128_f8f6f4 v[58:61], v[18:25], v[210:217], v[58:61], v194, v169 op_sel_hi:[0,0,0]
	v_mfma_scale_f32_16x16x128_f8f6f4 v[46:49], v[26:33], v[236:243], v[46:49], v194, v169 op_sel_hi:[0,0,0]
	v_mfma_scale_f32_16x16x128_f8f6f4 v[42:45], v[18:25], v[236:243], v[42:45], v194, v169 op_sel_hi:[0,0,0]
	s_setprio 0
	s_setprio 1
	v_mfma_scale_f32_16x16x128_f8f6f4 v[86:89], v[10:17], v[170:177], v[86:89], v194, v169 op_sel_hi:[0,0,0]
	v_mfma_scale_f32_16x16x128_f8f6f4 v[82:85], v[2:9], v[170:177], v[82:85], v194, v169 op_sel_hi:[0,0,0]
	v_mfma_scale_f32_16x16x128_f8f6f4 v[70:73], v[10:17], v[202:209], v[70:73], v194, v169 op_sel_hi:[0,0,0]
	v_mfma_scale_f32_16x16x128_f8f6f4 v[66:69], v[2:9], v[202:209], v[66:69], v194, v169 op_sel_hi:[0,0,0]
	v_mfma_scale_f32_16x16x128_f8f6f4 v[54:57], v[10:17], v[210:217], v[54:57], v194, v169 op_sel_hi:[0,0,0]
	v_mfma_scale_f32_16x16x128_f8f6f4 v[50:53], v[2:9], v[210:217], v[50:53], v194, v169 op_sel_hi:[0,0,0]
	v_mfma_scale_f32_16x16x128_f8f6f4 v[38:41], v[10:17], v[236:243], v[38:41], v194, v169 op_sel_hi:[0,0,0]
	v_mfma_scale_f32_16x16x128_f8f6f4 v[34:37], v[2:9], v[236:243], v[34:37], v194, v169 op_sel_hi:[0,0,0]
	s_setprio 0
	s_barrier
	s_add_u32 s35, s35, 0x100
	s_addc_u32 s45, s45, 0
	s_cmp_lt_i32 s75, s16
	s_mov_b64 s[18:19], s[42:43]
	s_mov_b32 s70, s75
	s_cbranch_scc1 .LBB0_1923
	s_branch .Lpeelexitph18

.Lpeelexitph18:
	v_mov_b32_e32 v209, v1
	s_andn2_b64 vcc, exec, s[58:59]
	s_cbranch_vccnz .LBB0_1926
